# shift sigmoid: precise expf expansion -> v_exp_f32 (122 sites, p2 only)
# speedup vs baseline: 1.0036x; 1.0036x over previous
.LBB0_372:
	s_or_b64 exec, exec, s[40:41]
	v_lshlrev_b64 v[132:133], 2, v[130:131]
	v_lshl_add_u64 v[126:127], s[22:23], 0, v[132:133]
	global_load_dwordx4 v[168:171], v[126:127], off offset:16
	s_nop 0
	global_load_dwordx4 v[126:129], v[126:127], off
	v_lshl_add_u64 v[132:133], s[28:29], 0, v[132:133]
	global_load_dwordx4 v[172:175], v[132:133], off offset:16
	global_load_dwordx4 v[176:179], v[132:133], off
	s_waitcnt vmcnt(4)
	v_lshlrev_b32_e32 v132, 16, v114
	v_and_b32_e32 v133, 0xffff0000, v114
	v_lshlrev_b32_e32 v180, 16, v118
	v_and_b32_e32 v181, 0xffff0000, v118
	v_lshlrev_b32_e32 v114, 16, v115
	v_and_b32_e32 v115, 0xffff0000, v115
	v_lshlrev_b32_e32 v118, 16, v119
	v_and_b32_e32 v119, 0xffff0000, v119
	v_lshlrev_b32_e32 v182, 16, v122
	v_and_b32_e32 v183, 0xffff0000, v122
	v_lshlrev_b32_e32 v122, 16, v123
	v_and_b32_e32 v123, 0xffff0000, v123
	v_pk_add_f32 v[118:119], v[118:119], v[114:115] neg_lo:[0,1] neg_hi:[0,1]
	v_pk_add_f32 v[180:181], v[180:181], v[132:133] neg_lo:[0,1] neg_hi:[0,1]
	v_cmp_lt_u32_e32 vcc, s71, v130
	s_waitcnt vmcnt(2)
	v_pk_fma_f32 v[118:119], v[118:119], v[128:129], v[114:115]
	v_pk_add_f32 v[114:115], v[122:123], v[114:115] neg_lo:[0,1] neg_hi:[0,1]
	v_lshlrev_b32_e32 v122, 16, v120
	s_waitcnt vmcnt(0)
	v_pk_fma_f32 v[114:115], v[114:115], v[178:179], v[118:119]
	v_lshlrev_b32_e32 v118, 16, v116
	v_and_b32_e32 v119, 0xffff0000, v116
	v_and_b32_e32 v123, 0xffff0000, v120
	v_lshlrev_b32_e32 v128, 16, v124
	v_and_b32_e32 v129, 0xffff0000, v124
	v_pk_add_f32 v[122:123], v[122:123], v[118:119] neg_lo:[0,1] neg_hi:[0,1]
	v_lshlrev_b32_e32 v116, 16, v117
	v_pk_fma_f32 v[122:123], v[122:123], v[168:169], v[118:119]
	v_pk_add_f32 v[118:119], v[128:129], v[118:119] neg_lo:[0,1] neg_hi:[0,1]
	v_and_b32_e32 v117, 0xffff0000, v117
	v_lshlrev_b32_e32 v120, 16, v121
	v_and_b32_e32 v121, 0xffff0000, v121
	v_pk_fma_f32 v[118:119], v[118:119], v[172:173], v[122:123]
	v_lshlrev_b32_e32 v122, 16, v125
	v_and_b32_e32 v123, 0xffff0000, v125
	v_pk_add_f32 v[120:121], v[120:121], v[116:117] neg_lo:[0,1] neg_hi:[0,1]
	v_pk_fma_f32 v[126:127], v[180:181], v[126:127], v[132:133]
	v_pk_add_f32 v[132:133], v[182:183], v[132:133] neg_lo:[0,1] neg_hi:[0,1]
	v_pk_fma_f32 v[120:121], v[120:121], v[170:171], v[116:117]
	v_pk_add_f32 v[116:117], v[122:123], v[116:117] neg_lo:[0,1] neg_hi:[0,1]
	v_pk_fma_f32 v[126:127], v[132:133], v[176:177], v[126:127]
	v_pk_fma_f32 v[116:117], v[116:117], v[174:175], v[120:121]
	s_and_saveexec_b64 s[40:41], vcc
	s_xor_b64 s[40:41], exec, s[40:41]
	s_cbranch_execz .LBB0_420
	v_cmp_lt_u32_e32 vcc, s72, v130
	s_and_saveexec_b64 s[42:43], vcc
	s_xor_b64 s[42:43], exec, s[42:43]
	s_cbranch_execz .LBB0_417
	v_cmp_lt_u32_e32 vcc, s73, v130
	s_and_saveexec_b64 s[44:45], vcc
	s_xor_b64 s[44:45], exec, s[44:45]
	s_cbranch_execz .LBB0_414
	v_cmp_lt_u32_e32 vcc, s76, v130
	s_and_saveexec_b64 s[46:47], vcc
	s_xor_b64 s[46:47], exec, s[46:47]
	s_cbranch_execz .LBB0_379
	v_cmp_lt_u32_e32 vcc, s77, v130
	s_and_saveexec_b64 s[48:49], vcc
	s_cbranch_execz .LBB0_378
	v_mul_f32_e32 v120, 0xbfb8aa3b, v126
	v_rndne_f32_e32 v121, v120
	v_sub_f32_e32 v122, v120, v121
	v_fma_f32 v120, v126, s78, -v120
	v_fmac_f32_e32 v120, 0xb2a5705f, v126
	v_add_f32_e32 v120, v122, v120
	v_exp_f32_e32 v120, v120
	v_cvt_i32_f32_e32 v121, v121
	v_cmp_nlt_f32_e32 vcc, s79, v126
	v_ldexp_f32 v120, v120, v121
	v_mul_f32_e32 v121, 0xbfb8aa3b, v127
	v_rndne_f32_e32 v122, v121
	v_sub_f32_e32 v123, v121, v122
	v_fma_f32 v121, v127, s78, -v121
	v_fmac_f32_e32 v121, 0xb2a5705f, v127
	v_add_f32_e32 v121, v123, v121
	v_exp_f32_e32 v121, v121
	v_cvt_i32_f32_e32 v122, v122
	v_cndmask_b32_e32 v120, 0, v120, vcc
	v_cmp_ngt_f32_e32 vcc, s80, v126
	v_ldexp_f32 v121, v121, v122
	v_mul_f32_e32 v122, 0xbfb8aa3b, v114
	v_rndne_f32_e32 v123, v122
	v_sub_f32_e32 v124, v122, v123
	v_fma_f32 v122, v114, s78, -v122
	v_fmac_f32_e32 v122, 0xb2a5705f, v114
	v_add_f32_e32 v122, v124, v122
	v_exp_f32_e32 v122, v122
	v_cvt_i32_f32_e32 v123, v123
	v_cndmask_b32_e32 v120, v143, v120, vcc
	v_cmp_nlt_f32_e32 vcc, s79, v127
	v_ldexp_f32 v122, v122, v123
	s_nop 0
	v_cndmask_b32_e32 v121, 0, v121, vcc
	v_cmp_ngt_f32_e32 vcc, s80, v127
	s_nop 1
	v_cndmask_b32_e32 v121, v143, v121, vcc
	v_cmp_nlt_f32_e32 vcc, s79, v114
	v_pk_add_f32 v[120:121], v[120:121], 1.0 op_sel_hi:[1,0]
	s_nop 0
	v_cndmask_b32_e32 v122, 0, v122, vcc
	v_cmp_ngt_f32_e32 vcc, s80, v114
	s_nop 1
	v_cndmask_b32_e32 v114, v143, v122, vcc
	v_mul_f32_e32 v122, 0xbfb8aa3b, v115
	v_exp_f32_e32 v115, v122
	s_nop 0
	v_pk_add_f32 v[114:115], v[114:115], 1.0 op_sel_hi:[1,0]
	v_mul_f32_e32 v122, 0xbfb8aa3b, v118
	v_exp_f32_e32 v118, v122
	s_nop 0
	v_mul_f32_e32 v122, 0xbfb8aa3b, v119
	v_exp_f32_e32 v119, v122
	s_nop 0
	v_pk_add_f32 v[118:119], v[118:119], 1.0 op_sel_hi:[1,0]
	v_mul_f32_e32 v122, 0xbfb8aa3b, v116
	v_exp_f32_e32 v116, v122
	s_nop 0
	v_mul_f32_e32 v122, 0xbfb8aa3b, v117
	v_exp_f32_e32 v117, v122
	s_nop 0
	v_div_scale_f32 v122, s[74:75], v120, v120, 1.0
	v_rcp_f32_e32 v123, v122
	v_pk_add_f32 v[116:117], v[116:117], 1.0 op_sel_hi:[1,0]
	v_fma_f32 v124, -v122, v123, 1.0
	v_fmac_f32_e32 v123, v124, v123
	v_div_scale_f32 v124, vcc, 1.0, v120, 1.0
	v_mul_f32_e32 v125, v124, v123
	v_fma_f32 v126, -v122, v125, v124
	v_fmac_f32_e32 v125, v126, v123
	v_fma_f32 v122, -v122, v125, v124
	v_div_fmas_f32 v122, v122, v123, v125
	v_div_fixup_f32 v126, v122, v120, 1.0
	v_rcp_f32_e32 v127, v121
	s_nop 3
	v_rcp_f32_e32 v114, v114
	s_nop 3
	v_rcp_f32_e32 v115, v115
	s_nop 3
	v_rcp_f32_e32 v118, v118
	s_nop 3
	v_rcp_f32_e32 v119, v119
	s_nop 3
	v_rcp_f32_e32 v116, v116
	s_nop 3
	v_div_scale_f32 v120, s[74:75], v117, v117, 1.0
	v_rcp_f32_e32 v121, v120
	s_nop 0
	v_fma_f32 v122, -v120, v121, 1.0
	v_fmac_f32_e32 v121, v122, v121
	v_div_scale_f32 v122, vcc, 1.0, v117, 1.0
	v_mul_f32_e32 v123, v122, v121
	v_fma_f32 v124, -v120, v123, v122
	v_fmac_f32_e32 v123, v124, v121
	v_fma_f32 v120, -v120, v123, v122
	v_div_fmas_f32 v120, v120, v121, v123
	v_div_fixup_f32 v117, v120, v117, 1.0

.LBB0_429:
	v_add_u32_e32 v130, v120, v165
	v_lshlrev_b64 v[114:115], 2, v[130:131]
	v_lshl_add_u64 v[122:123], s[22:23], 0, v[114:115]
	global_load_dwordx4 v[116:119], v[122:123], off offset:16
	s_nop 0
	global_load_dwordx4 v[122:125], v[122:123], off
	v_lshl_add_u64 v[114:115], s[28:29], 0, v[114:115]
	v_lshrrev_b32_e32 v121, 2, v166
	global_load_dwordx4 v[126:129], v[114:115], off offset:16
	global_load_dwordx4 v[164:167], v[114:115], off
	v_lshlrev_b32_e32 v114, 16, v10
	v_and_b32_e32 v115, 0xffff0000, v10
	v_lshlrev_b32_e32 v132, 16, v110
	v_and_b32_e32 v133, 0xffff0000, v110
	v_lshlrev_b32_e32 v168, 16, v38
	v_and_b32_e32 v169, 0xffff0000, v38
	v_pk_add_f32 v[132:133], v[132:133], v[114:115] neg_lo:[0,1] neg_hi:[0,1]
	v_lshlrev_b32_e32 v110, 16, v111
	v_and_b32_e32 v111, 0xffff0000, v111
	v_cmp_lt_u32_e32 vcc, s71, v130
	s_waitcnt vmcnt(2)
	v_pk_fma_f32 v[122:123], v[132:133], v[122:123], v[114:115]
	v_pk_add_f32 v[114:115], v[168:169], v[114:115] neg_lo:[0,1] neg_hi:[0,1]
	v_lshlrev_b32_e32 v132, 16, v39
	s_waitcnt vmcnt(0)
	v_pk_fma_f32 v[114:115], v[114:115], v[164:165], v[122:123]
	v_lshlrev_b32_e32 v122, 16, v11
	v_and_b32_e32 v123, 0xffff0000, v11
	v_and_b32_e32 v133, 0xffff0000, v39
	v_pk_add_f32 v[110:111], v[110:111], v[122:123] neg_lo:[0,1] neg_hi:[0,1]
	s_nop 0
	v_pk_fma_f32 v[110:111], v[110:111], v[124:125], v[122:123]
	v_pk_add_f32 v[122:123], v[132:133], v[122:123] neg_lo:[0,1] neg_hi:[0,1]
	v_lshlrev_b32_e32 v124, 16, v112
	v_pk_fma_f32 v[110:111], v[122:123], v[166:167], v[110:111]
	v_lshlrev_b32_e32 v122, 16, v12
	v_and_b32_e32 v123, 0xffff0000, v12
	v_and_b32_e32 v125, 0xffff0000, v112
	v_lshlrev_b32_e32 v132, 16, v40
	v_and_b32_e32 v133, 0xffff0000, v40
	v_pk_add_f32 v[124:125], v[124:125], v[122:123] neg_lo:[0,1] neg_hi:[0,1]
	v_lshlrev_b32_e32 v112, 16, v113
	v_pk_fma_f32 v[116:117], v[124:125], v[116:117], v[122:123]
	v_pk_add_f32 v[122:123], v[132:133], v[122:123] neg_lo:[0,1] neg_hi:[0,1]
	v_and_b32_e32 v113, 0xffff0000, v113
	v_pk_fma_f32 v[116:117], v[122:123], v[126:127], v[116:117]
	v_lshlrev_b32_e32 v122, 16, v13
	v_and_b32_e32 v123, 0xffff0000, v13
	v_lshlrev_b32_e32 v124, 16, v41
	v_and_b32_e32 v125, 0xffff0000, v41
	v_pk_add_f32 v[112:113], v[112:113], v[122:123] neg_lo:[0,1] neg_hi:[0,1]
	s_nop 0
	v_pk_fma_f32 v[112:113], v[112:113], v[118:119], v[122:123]
	v_pk_add_f32 v[118:119], v[124:125], v[122:123] neg_lo:[0,1] neg_hi:[0,1]
	s_nop 0
	v_pk_fma_f32 v[112:113], v[118:119], v[128:129], v[112:113]
	s_and_saveexec_b64 s[18:19], vcc
	s_xor_b64 s[18:19], exec, s[18:19]
	s_cbranch_execz .LBB0_477
	v_cmp_lt_u32_e32 vcc, s72, v130
	s_and_saveexec_b64 s[42:43], vcc
	s_xor_b64 s[42:43], exec, s[42:43]
	s_cbranch_execz .LBB0_474
	v_cmp_lt_u32_e32 vcc, s73, v130
	s_and_saveexec_b64 s[44:45], vcc
	s_xor_b64 s[44:45], exec, s[44:45]
	s_cbranch_execz .LBB0_471
	v_cmp_lt_u32_e32 vcc, s76, v130
	s_and_saveexec_b64 s[46:47], vcc
	s_xor_b64 s[46:47], exec, s[46:47]
	s_cbranch_execz .LBB0_436
	v_cmp_lt_u32_e32 vcc, s77, v130
	s_and_saveexec_b64 s[48:49], vcc
	s_cbranch_execz .LBB0_435
	v_mul_f32_e32 v118, 0xbfb8aa3b, v114
	v_exp_f32_e32 v114, v118
	s_nop 0
	v_mul_f32_e32 v118, 0xbfb8aa3b, v115
	v_exp_f32_e32 v115, v118
	s_nop 0
	v_pk_add_f32 v[114:115], v[114:115], 1.0 op_sel_hi:[1,0]
	v_mul_f32_e32 v118, 0xbfb8aa3b, v110
	v_exp_f32_e32 v110, v118
	s_nop 0
	v_mul_f32_e32 v118, 0xbfb8aa3b, v111
	v_exp_f32_e32 v111, v118
	s_nop 0
	v_pk_add_f32 v[110:111], v[110:111], 1.0 op_sel_hi:[1,0]
	v_mul_f32_e32 v118, 0xbfb8aa3b, v116
	v_exp_f32_e32 v116, v118
	s_nop 0
	v_mul_f32_e32 v118, 0xbfb8aa3b, v117
	v_exp_f32_e32 v117, v118
	s_nop 0
	v_pk_add_f32 v[116:117], v[116:117], 1.0 op_sel_hi:[1,0]
	v_mul_f32_e32 v118, 0xbfb8aa3b, v112
	v_exp_f32_e32 v112, v118
	s_nop 0
	v_mul_f32_e32 v118, 0xbfb8aa3b, v113
	v_exp_f32_e32 v113, v118
	s_nop 0
	v_div_scale_f32 v118, s[74:75], v114, v114, 1.0
	v_rcp_f32_e32 v119, v118
	v_pk_add_f32 v[112:113], v[112:113], 1.0 op_sel_hi:[1,0]
	v_fma_f32 v122, -v118, v119, 1.0
	v_fmac_f32_e32 v119, v122, v119
	v_div_scale_f32 v122, vcc, 1.0, v114, 1.0
	v_mul_f32_e32 v123, v122, v119
	v_fma_f32 v124, -v118, v123, v122
	v_fmac_f32_e32 v123, v124, v119
	v_fma_f32 v118, -v118, v123, v122
	v_div_fmas_f32 v118, v118, v119, v123
	v_div_fixup_f32 v114, v118, v114, 1.0
	v_rcp_f32_e32 v115, v115
	s_nop 3
	v_rcp_f32_e32 v110, v110
	s_nop 3
	v_rcp_f32_e32 v111, v111
	s_nop 3
	v_rcp_f32_e32 v116, v116
	s_nop 3
	v_rcp_f32_e32 v117, v117
	s_nop 3
	v_rcp_f32_e32 v112, v112
	s_nop 3
	v_div_scale_f32 v118, s[74:75], v113, v113, 1.0
	v_rcp_f32_e32 v119, v118
	s_nop 0
	v_fma_f32 v122, -v118, v119, 1.0
	v_fmac_f32_e32 v119, v122, v119
	v_div_scale_f32 v122, vcc, 1.0, v113, 1.0
	v_mul_f32_e32 v123, v122, v119
	v_fma_f32 v124, -v118, v123, v122
	v_fmac_f32_e32 v123, v124, v119
	v_fma_f32 v118, -v118, v123, v122
	v_div_fmas_f32 v118, v118, v119, v123
	v_div_fixup_f32 v113, v118, v113, 1.0

.LBB0_480:
	v_add_u32_e32 v130, v120, v162
	v_lshlrev_b64 v[110:111], 2, v[130:131]
	v_lshl_add_u64 v[118:119], s[22:23], 0, v[110:111]
	global_load_dwordx4 v[112:115], v[118:119], off offset:16
	global_load_dwordx4 v[122:125], v[118:119], off
	v_lshl_add_u64 v[110:111], s[28:29], 0, v[110:111]
	v_lshrrev_b32_e32 v116, 2, v163
	global_load_dwordx4 v[126:129], v[110:111], off offset:16
	global_load_dwordx4 v[162:165], v[110:111], off
	v_lshlrev_b32_e32 v110, 16, v6
	v_and_b32_e32 v111, 0xffff0000, v6
	v_lshlrev_b32_e32 v118, 16, v106
	v_and_b32_e32 v119, 0xffff0000, v106
	v_lshlrev_b32_e32 v132, 16, v34
	v_and_b32_e32 v133, 0xffff0000, v34
	v_pk_add_f32 v[118:119], v[118:119], v[110:111] neg_lo:[0,1] neg_hi:[0,1]
	v_lshlrev_b32_e32 v106, 16, v107
	v_and_b32_e32 v107, 0xffff0000, v107
	v_cmp_lt_u32_e32 vcc, s71, v130
	s_waitcnt vmcnt(2)
	v_pk_fma_f32 v[118:119], v[118:119], v[122:123], v[110:111]
	v_pk_add_f32 v[110:111], v[132:133], v[110:111] neg_lo:[0,1] neg_hi:[0,1]
	v_lshlrev_b32_e32 v122, 16, v35
	s_waitcnt vmcnt(0)
	v_pk_fma_f32 v[110:111], v[110:111], v[162:163], v[118:119]
	v_lshlrev_b32_e32 v118, 16, v7
	v_and_b32_e32 v119, 0xffff0000, v7
	v_and_b32_e32 v123, 0xffff0000, v35
	v_pk_add_f32 v[106:107], v[106:107], v[118:119] neg_lo:[0,1] neg_hi:[0,1]
	s_nop 0
	v_pk_fma_f32 v[106:107], v[106:107], v[124:125], v[118:119]
	v_pk_add_f32 v[118:119], v[122:123], v[118:119] neg_lo:[0,1] neg_hi:[0,1]
	v_lshlrev_b32_e32 v122, 16, v108
	v_pk_fma_f32 v[106:107], v[118:119], v[164:165], v[106:107]
	v_lshlrev_b32_e32 v118, 16, v8
	v_and_b32_e32 v119, 0xffff0000, v8
	v_and_b32_e32 v123, 0xffff0000, v108
	v_lshlrev_b32_e32 v124, 16, v36
	v_and_b32_e32 v125, 0xffff0000, v36
	v_pk_add_f32 v[122:123], v[122:123], v[118:119] neg_lo:[0,1] neg_hi:[0,1]
	v_lshlrev_b32_e32 v108, 16, v109
	v_pk_fma_f32 v[112:113], v[122:123], v[112:113], v[118:119]
	v_pk_add_f32 v[118:119], v[124:125], v[118:119] neg_lo:[0,1] neg_hi:[0,1]
	v_and_b32_e32 v109, 0xffff0000, v109
	v_pk_fma_f32 v[112:113], v[118:119], v[126:127], v[112:113]
	v_lshlrev_b32_e32 v118, 16, v9
	v_and_b32_e32 v119, 0xffff0000, v9
	v_lshlrev_b32_e32 v122, 16, v37
	v_and_b32_e32 v123, 0xffff0000, v37
	v_pk_add_f32 v[108:109], v[108:109], v[118:119] neg_lo:[0,1] neg_hi:[0,1]
	s_nop 0
	v_pk_fma_f32 v[108:109], v[108:109], v[114:115], v[118:119]
	v_pk_add_f32 v[114:115], v[122:123], v[118:119] neg_lo:[0,1] neg_hi:[0,1]
	s_nop 0
	v_pk_fma_f32 v[108:109], v[114:115], v[128:129], v[108:109]
	s_and_saveexec_b64 s[16:17], vcc
	s_xor_b64 s[16:17], exec, s[16:17]
	s_cbranch_execz .LBB0_528
	v_cmp_lt_u32_e32 vcc, s72, v130
	s_and_saveexec_b64 s[40:41], vcc
	s_xor_b64 s[40:41], exec, s[40:41]
	s_cbranch_execz .LBB0_525
	v_cmp_lt_u32_e32 vcc, s73, v130
	s_and_saveexec_b64 s[42:43], vcc
	s_xor_b64 s[42:43], exec, s[42:43]
	s_cbranch_execz .LBB0_522
	v_cmp_lt_u32_e32 vcc, s76, v130
	s_and_saveexec_b64 s[44:45], vcc
	s_xor_b64 s[44:45], exec, s[44:45]
	s_cbranch_execz .LBB0_487
	v_cmp_lt_u32_e32 vcc, s77, v130
	s_and_saveexec_b64 s[46:47], vcc
	s_cbranch_execz .LBB0_486
	v_mul_f32_e32 v114, 0xbfb8aa3b, v110
	v_exp_f32_e32 v110, v114
	s_nop 0
	v_mul_f32_e32 v114, 0xbfb8aa3b, v111
	v_exp_f32_e32 v111, v114
	s_nop 0
	v_pk_add_f32 v[110:111], v[110:111], 1.0 op_sel_hi:[1,0]
	v_mul_f32_e32 v114, 0xbfb8aa3b, v106
	v_exp_f32_e32 v106, v114
	s_nop 0
	v_mul_f32_e32 v114, 0xbfb8aa3b, v107
	v_exp_f32_e32 v107, v114
	s_nop 0
	v_pk_add_f32 v[106:107], v[106:107], 1.0 op_sel_hi:[1,0]
	v_mul_f32_e32 v114, 0xbfb8aa3b, v112
	v_exp_f32_e32 v112, v114
	s_nop 0
	v_mul_f32_e32 v114, 0xbfb8aa3b, v113
	v_exp_f32_e32 v113, v114
	s_nop 0
	v_pk_add_f32 v[112:113], v[112:113], 1.0 op_sel_hi:[1,0]
	v_mul_f32_e32 v114, 0xbfb8aa3b, v108
	v_exp_f32_e32 v108, v114
	s_nop 0
	v_mul_f32_e32 v114, 0xbfb8aa3b, v109
	v_exp_f32_e32 v109, v114
	s_nop 0
	v_div_scale_f32 v114, s[48:49], v110, v110, 1.0
	v_rcp_f32_e32 v115, v114
	v_pk_add_f32 v[108:109], v[108:109], 1.0 op_sel_hi:[1,0]
	v_fma_f32 v117, -v114, v115, 1.0
	v_fmac_f32_e32 v115, v117, v115
	v_div_scale_f32 v117, vcc, 1.0, v110, 1.0
	v_mul_f32_e32 v118, v117, v115
	v_fma_f32 v119, -v114, v118, v117
	v_fmac_f32_e32 v118, v119, v115
	v_fma_f32 v114, -v114, v118, v117
	v_div_fmas_f32 v114, v114, v115, v118
	v_div_fixup_f32 v110, v114, v110, 1.0
	v_rcp_f32_e32 v111, v111
	s_nop 3
	v_rcp_f32_e32 v106, v106
	s_nop 3
	v_rcp_f32_e32 v107, v107
	s_nop 3
	v_rcp_f32_e32 v112, v112
	s_nop 3
	v_rcp_f32_e32 v113, v113
	s_nop 3
	v_rcp_f32_e32 v108, v108
	s_nop 3
	v_div_scale_f32 v114, s[48:49], v109, v109, 1.0
	v_rcp_f32_e32 v115, v114
	s_nop 0
	v_fma_f32 v117, -v114, v115, 1.0
	v_fmac_f32_e32 v115, v117, v115
	v_div_scale_f32 v117, vcc, 1.0, v109, 1.0
	v_mul_f32_e32 v118, v117, v115
	v_fma_f32 v119, -v114, v118, v117
	v_fmac_f32_e32 v118, v119, v115
	v_fma_f32 v114, -v114, v118, v117
	v_div_fmas_f32 v114, v114, v115, v118
	v_div_fixup_f32 v109, v114, v109, 1.0

.LBB0_531:
	v_add_u32_e32 v130, v120, v159
	v_lshlrev_b64 v[106:107], 2, v[130:131]
	v_lshl_add_u64 v[114:115], s[22:23], 0, v[106:107]
	global_load_dwordx4 v[108:111], v[114:115], off offset:16
	s_nop 0
	global_load_dwordx4 v[114:117], v[114:115], off
	v_lshl_add_u64 v[106:107], s[28:29], 0, v[106:107]
	global_load_dwordx4 v[122:125], v[106:107], off offset:16
	global_load_dwordx4 v[126:129], v[106:107], off
	v_lshlrev_b32_e32 v106, 16, v2
	v_and_b32_e32 v107, 0xffff0000, v2
	v_lshlrev_b32_e32 v118, 16, v102
	v_and_b32_e32 v119, 0xffff0000, v102
	v_lshlrev_b32_e32 v132, 16, v30
	v_and_b32_e32 v133, 0xffff0000, v30
	v_pk_add_f32 v[118:119], v[118:119], v[106:107] neg_lo:[0,1] neg_hi:[0,1]
	v_lshlrev_b32_e32 v102, 16, v103
	v_and_b32_e32 v103, 0xffff0000, v103
	v_lshrrev_b32_e32 v112, 2, v160
	v_cmp_lt_u32_e32 vcc, s71, v130
	s_waitcnt vmcnt(2)
	v_pk_fma_f32 v[114:115], v[118:119], v[114:115], v[106:107]
	v_pk_add_f32 v[106:107], v[132:133], v[106:107] neg_lo:[0,1] neg_hi:[0,1]
	v_lshlrev_b32_e32 v118, 16, v31
	s_waitcnt vmcnt(0)
	v_pk_fma_f32 v[106:107], v[106:107], v[126:127], v[114:115]
	v_lshlrev_b32_e32 v114, 16, v3
	v_and_b32_e32 v115, 0xffff0000, v3
	v_and_b32_e32 v119, 0xffff0000, v31
	v_pk_add_f32 v[102:103], v[102:103], v[114:115] neg_lo:[0,1] neg_hi:[0,1]
	s_nop 0
	v_pk_fma_f32 v[102:103], v[102:103], v[116:117], v[114:115]
	v_pk_add_f32 v[114:115], v[118:119], v[114:115] neg_lo:[0,1] neg_hi:[0,1]
	v_lshlrev_b32_e32 v116, 16, v104
	v_pk_fma_f32 v[102:103], v[114:115], v[128:129], v[102:103]
	v_lshlrev_b32_e32 v114, 16, v4
	v_and_b32_e32 v115, 0xffff0000, v4
	v_and_b32_e32 v117, 0xffff0000, v104
	v_lshlrev_b32_e32 v118, 16, v32
	v_and_b32_e32 v119, 0xffff0000, v32
	v_pk_add_f32 v[116:117], v[116:117], v[114:115] neg_lo:[0,1] neg_hi:[0,1]
	v_lshlrev_b32_e32 v104, 16, v105
	v_pk_fma_f32 v[108:109], v[116:117], v[108:109], v[114:115]
	v_pk_add_f32 v[114:115], v[118:119], v[114:115] neg_lo:[0,1] neg_hi:[0,1]
	v_and_b32_e32 v105, 0xffff0000, v105
	v_pk_fma_f32 v[108:109], v[114:115], v[122:123], v[108:109]
	v_lshlrev_b32_e32 v114, 16, v5
	v_and_b32_e32 v115, 0xffff0000, v5
	v_lshlrev_b32_e32 v116, 16, v33
	v_and_b32_e32 v117, 0xffff0000, v33
	v_pk_add_f32 v[104:105], v[104:105], v[114:115] neg_lo:[0,1] neg_hi:[0,1]
	s_nop 0
	v_pk_fma_f32 v[104:105], v[104:105], v[110:111], v[114:115]
	v_pk_add_f32 v[110:111], v[116:117], v[114:115] neg_lo:[0,1] neg_hi:[0,1]
	s_nop 0
	v_pk_fma_f32 v[104:105], v[110:111], v[124:125], v[104:105]
	s_and_saveexec_b64 s[14:15], vcc
	s_xor_b64 s[14:15], exec, s[14:15]
	s_cbranch_execz .LBB0_579
	v_cmp_lt_u32_e32 vcc, s72, v130
	s_and_saveexec_b64 s[18:19], vcc
	s_xor_b64 s[18:19], exec, s[18:19]
	s_cbranch_execz .LBB0_576
	v_cmp_lt_u32_e32 vcc, s73, v130
	s_and_saveexec_b64 s[40:41], vcc
	s_xor_b64 s[40:41], exec, s[40:41]
	s_cbranch_execz .LBB0_573
	v_cmp_lt_u32_e32 vcc, s76, v130
	s_and_saveexec_b64 s[42:43], vcc
	s_xor_b64 s[42:43], exec, s[42:43]
	s_cbranch_execz .LBB0_538
	v_cmp_lt_u32_e32 vcc, s77, v130
	s_and_saveexec_b64 s[44:45], vcc
	s_cbranch_execz .LBB0_537
	v_mul_f32_e32 v110, 0xbfb8aa3b, v106
	v_exp_f32_e32 v106, v110
	s_nop 0
	v_mul_f32_e32 v110, 0xbfb8aa3b, v107
	v_exp_f32_e32 v107, v110
	s_nop 0
	v_pk_add_f32 v[106:107], v[106:107], 1.0 op_sel_hi:[1,0]
	v_mul_f32_e32 v110, 0xbfb8aa3b, v102
	v_exp_f32_e32 v102, v110
	s_nop 0
	v_mul_f32_e32 v110, 0xbfb8aa3b, v103
	v_exp_f32_e32 v103, v110
	s_nop 0
	v_pk_add_f32 v[102:103], v[102:103], 1.0 op_sel_hi:[1,0]
	v_mul_f32_e32 v110, 0xbfb8aa3b, v108
	v_exp_f32_e32 v108, v110
	s_nop 0
	v_mul_f32_e32 v110, 0xbfb8aa3b, v109
	v_exp_f32_e32 v109, v110
	s_nop 0
	v_pk_add_f32 v[108:109], v[108:109], 1.0 op_sel_hi:[1,0]
	v_mul_f32_e32 v110, 0xbfb8aa3b, v104
	v_exp_f32_e32 v104, v110
	s_nop 0
	v_mul_f32_e32 v110, 0xbfb8aa3b, v105
	v_exp_f32_e32 v105, v110
	s_nop 0
	v_div_scale_f32 v110, s[46:47], v106, v106, 1.0
	v_rcp_f32_e32 v111, v110
	v_pk_add_f32 v[104:105], v[104:105], 1.0 op_sel_hi:[1,0]
	v_fma_f32 v113, -v110, v111, 1.0
	v_fmac_f32_e32 v111, v113, v111
	v_div_scale_f32 v113, vcc, 1.0, v106, 1.0
	v_mul_f32_e32 v114, v113, v111
	v_fma_f32 v115, -v110, v114, v113
	v_fmac_f32_e32 v114, v115, v111
	v_fma_f32 v110, -v110, v114, v113
	v_div_fmas_f32 v110, v110, v111, v114
	v_div_fixup_f32 v106, v110, v106, 1.0
	v_rcp_f32_e32 v107, v107
	s_nop 3
	v_rcp_f32_e32 v102, v102
	s_nop 3
	v_rcp_f32_e32 v103, v103
	s_nop 3
	v_rcp_f32_e32 v108, v108
	s_nop 3
	v_rcp_f32_e32 v109, v109
	s_nop 3
	v_rcp_f32_e32 v104, v104
	s_nop 3
	v_div_scale_f32 v110, s[46:47], v105, v105, 1.0
	v_rcp_f32_e32 v111, v110
	s_nop 0
	v_fma_f32 v113, -v110, v111, 1.0
	v_fmac_f32_e32 v111, v113, v111
	v_div_scale_f32 v113, vcc, 1.0, v105, 1.0
	v_mul_f32_e32 v114, v113, v111
	v_fma_f32 v115, -v110, v114, v113
	v_fmac_f32_e32 v114, v115, v111
	v_fma_f32 v110, -v110, v114, v113
	v_div_fmas_f32 v110, v110, v111, v114
	v_div_fixup_f32 v105, v110, v105, 1.0

.LBB0_582:
	v_add_u32_e32 v130, v120, v156
	v_lshlrev_b64 v[102:103], 2, v[130:131]
	v_lshl_add_u64 v[110:111], s[22:23], 0, v[102:103]
	global_load_dwordx4 v[104:107], v[110:111], off offset:16
	s_nop 0
	global_load_dwordx4 v[110:113], v[110:111], off
	v_lshl_add_u64 v[102:103], s[28:29], 0, v[102:103]
	global_load_dwordx4 v[114:117], v[102:103], off offset:16
	global_load_dwordx4 v[122:125], v[102:103], off
	v_lshlrev_b32_e32 v102, 16, v14
	v_and_b32_e32 v103, 0xffff0000, v14
	v_lshlrev_b32_e32 v118, 16, v98
	v_and_b32_e32 v119, 0xffff0000, v98
	v_lshlrev_b32_e32 v126, 16, v46
	v_and_b32_e32 v127, 0xffff0000, v46
	v_pk_add_f32 v[118:119], v[118:119], v[102:103] neg_lo:[0,1] neg_hi:[0,1]
	v_lshlrev_b32_e32 v98, 16, v99
	v_and_b32_e32 v99, 0xffff0000, v99
	v_lshrrev_b32_e32 v108, 2, v157
	v_cmp_lt_u32_e32 vcc, s71, v130
	s_waitcnt vmcnt(2)
	v_pk_fma_f32 v[110:111], v[118:119], v[110:111], v[102:103]
	v_pk_add_f32 v[102:103], v[126:127], v[102:103] neg_lo:[0,1] neg_hi:[0,1]
	v_lshlrev_b32_e32 v118, 16, v47
	s_waitcnt vmcnt(0)
	v_pk_fma_f32 v[102:103], v[102:103], v[122:123], v[110:111]
	v_lshlrev_b32_e32 v110, 16, v15
	v_and_b32_e32 v111, 0xffff0000, v15
	v_and_b32_e32 v119, 0xffff0000, v47
	v_pk_add_f32 v[98:99], v[98:99], v[110:111] neg_lo:[0,1] neg_hi:[0,1]
	s_nop 0
	v_pk_fma_f32 v[98:99], v[98:99], v[112:113], v[110:111]
	v_pk_add_f32 v[110:111], v[118:119], v[110:111] neg_lo:[0,1] neg_hi:[0,1]
	v_lshlrev_b32_e32 v112, 16, v100
	v_pk_fma_f32 v[98:99], v[110:111], v[124:125], v[98:99]
	v_lshlrev_b32_e32 v110, 16, v16
	v_and_b32_e32 v111, 0xffff0000, v16
	v_and_b32_e32 v113, 0xffff0000, v100
	v_lshlrev_b32_e32 v118, 16, v48
	v_and_b32_e32 v119, 0xffff0000, v48
	v_pk_add_f32 v[112:113], v[112:113], v[110:111] neg_lo:[0,1] neg_hi:[0,1]
	v_lshlrev_b32_e32 v100, 16, v101
	v_pk_fma_f32 v[104:105], v[112:113], v[104:105], v[110:111]
	v_pk_add_f32 v[110:111], v[118:119], v[110:111] neg_lo:[0,1] neg_hi:[0,1]
	v_and_b32_e32 v101, 0xffff0000, v101
	v_pk_fma_f32 v[104:105], v[110:111], v[114:115], v[104:105]
	v_lshlrev_b32_e32 v110, 16, v17
	v_and_b32_e32 v111, 0xffff0000, v17
	v_lshlrev_b32_e32 v112, 16, v49
	v_and_b32_e32 v113, 0xffff0000, v49
	v_pk_add_f32 v[100:101], v[100:101], v[110:111] neg_lo:[0,1] neg_hi:[0,1]
	s_nop 0
	v_pk_fma_f32 v[100:101], v[100:101], v[106:107], v[110:111]
	v_pk_add_f32 v[106:107], v[112:113], v[110:111] neg_lo:[0,1] neg_hi:[0,1]
	s_nop 0
	v_pk_fma_f32 v[100:101], v[106:107], v[116:117], v[100:101]
	s_and_saveexec_b64 s[12:13], vcc
	s_xor_b64 s[12:13], exec, s[12:13]
	s_cbranch_execz .LBB0_630
	v_cmp_lt_u32_e32 vcc, s72, v130
	s_and_saveexec_b64 s[16:17], vcc
	s_xor_b64 s[16:17], exec, s[16:17]
	s_cbranch_execz .LBB0_627
	v_cmp_lt_u32_e32 vcc, s73, v130
	s_and_saveexec_b64 s[18:19], vcc
	s_xor_b64 s[18:19], exec, s[18:19]
	s_cbranch_execz .LBB0_624
	v_cmp_lt_u32_e32 vcc, s76, v130
	s_and_saveexec_b64 s[40:41], vcc
	s_xor_b64 s[40:41], exec, s[40:41]
	s_cbranch_execz .LBB0_589
	v_cmp_lt_u32_e32 vcc, s77, v130
	s_and_saveexec_b64 s[42:43], vcc
	s_cbranch_execz .LBB0_588
	v_mul_f32_e32 v106, 0xbfb8aa3b, v102
	v_exp_f32_e32 v102, v106
	s_nop 0
	v_mul_f32_e32 v106, 0xbfb8aa3b, v103
	v_exp_f32_e32 v103, v106
	s_nop 0
	v_pk_add_f32 v[102:103], v[102:103], 1.0 op_sel_hi:[1,0]
	v_mul_f32_e32 v106, 0xbfb8aa3b, v98
	v_exp_f32_e32 v98, v106
	s_nop 0
	v_mul_f32_e32 v106, 0xbfb8aa3b, v99
	v_exp_f32_e32 v99, v106
	s_nop 0
	v_pk_add_f32 v[98:99], v[98:99], 1.0 op_sel_hi:[1,0]
	v_mul_f32_e32 v106, 0xbfb8aa3b, v104
	v_exp_f32_e32 v104, v106
	s_nop 0
	v_mul_f32_e32 v106, 0xbfb8aa3b, v105
	v_exp_f32_e32 v105, v106
	s_nop 0
	v_pk_add_f32 v[104:105], v[104:105], 1.0 op_sel_hi:[1,0]
	v_mul_f32_e32 v106, 0xbfb8aa3b, v100
	v_exp_f32_e32 v100, v106
	s_nop 0
	v_mul_f32_e32 v106, 0xbfb8aa3b, v101
	v_exp_f32_e32 v101, v106
	s_nop 0
	v_div_scale_f32 v106, s[44:45], v102, v102, 1.0
	v_rcp_f32_e32 v107, v106
	v_pk_add_f32 v[100:101], v[100:101], 1.0 op_sel_hi:[1,0]
	v_fma_f32 v109, -v106, v107, 1.0
	v_fmac_f32_e32 v107, v109, v107
	v_div_scale_f32 v109, vcc, 1.0, v102, 1.0
	v_mul_f32_e32 v110, v109, v107
	v_fma_f32 v111, -v106, v110, v109
	v_fmac_f32_e32 v110, v111, v107
	v_fma_f32 v106, -v106, v110, v109
	v_div_fmas_f32 v106, v106, v107, v110
	v_div_fixup_f32 v102, v106, v102, 1.0
	v_rcp_f32_e32 v103, v103
	s_nop 3
	v_rcp_f32_e32 v98, v98
	s_nop 3
	v_rcp_f32_e32 v99, v99
	s_nop 3
	v_rcp_f32_e32 v104, v104
	s_nop 3
	v_rcp_f32_e32 v105, v105
	s_nop 3
	v_rcp_f32_e32 v100, v100
	s_nop 3
	v_div_scale_f32 v106, s[44:45], v101, v101, 1.0
	v_rcp_f32_e32 v107, v106
	s_nop 0
	v_fma_f32 v109, -v106, v107, 1.0
	v_fmac_f32_e32 v107, v109, v107
	v_div_scale_f32 v109, vcc, 1.0, v101, 1.0
	v_mul_f32_e32 v110, v109, v107
	v_fma_f32 v111, -v106, v110, v109
	v_fmac_f32_e32 v110, v111, v107
	v_fma_f32 v106, -v106, v110, v109
	v_div_fmas_f32 v106, v106, v107, v110
	v_div_fixup_f32 v101, v106, v101, 1.0

.LBB0_633:
	v_add_u32_e32 v130, v120, v153
	v_lshlrev_b64 v[98:99], 2, v[130:131]
	v_lshl_add_u64 v[106:107], s[22:23], 0, v[98:99]
	global_load_dwordx4 v[100:103], v[106:107], off offset:16
	s_nop 0
	global_load_dwordx4 v[106:109], v[106:107], off
	v_lshl_add_u64 v[98:99], s[28:29], 0, v[98:99]
	global_load_dwordx4 v[110:113], v[98:99], off offset:16
	global_load_dwordx4 v[114:117], v[98:99], off
	v_lshlrev_b32_e32 v98, 16, v18
	v_and_b32_e32 v99, 0xffff0000, v18
	v_lshlrev_b32_e32 v118, 16, v94
	v_and_b32_e32 v119, 0xffff0000, v94
	v_lshlrev_b32_e32 v122, 16, v54
	v_and_b32_e32 v123, 0xffff0000, v54
	v_pk_add_f32 v[118:119], v[118:119], v[98:99] neg_lo:[0,1] neg_hi:[0,1]
	v_lshlrev_b32_e32 v94, 16, v95
	v_and_b32_e32 v95, 0xffff0000, v95
	v_lshrrev_b32_e32 v104, 2, v154
	v_cmp_lt_u32_e32 vcc, s71, v130
	s_waitcnt vmcnt(2)
	v_pk_fma_f32 v[106:107], v[118:119], v[106:107], v[98:99]
	v_pk_add_f32 v[98:99], v[122:123], v[98:99] neg_lo:[0,1] neg_hi:[0,1]
	s_waitcnt vmcnt(0)
	v_pk_fma_f32 v[98:99], v[98:99], v[114:115], v[106:107]
	v_lshlrev_b32_e32 v106, 16, v19
	v_and_b32_e32 v107, 0xffff0000, v19
	v_lshlrev_b32_e32 v114, 16, v55
	v_and_b32_e32 v115, 0xffff0000, v55
	v_pk_add_f32 v[94:95], v[94:95], v[106:107] neg_lo:[0,1] neg_hi:[0,1]
	s_nop 0
	v_pk_fma_f32 v[94:95], v[94:95], v[108:109], v[106:107]
	v_pk_add_f32 v[106:107], v[114:115], v[106:107] neg_lo:[0,1] neg_hi:[0,1]
	v_lshlrev_b32_e32 v108, 16, v96
	v_pk_fma_f32 v[94:95], v[106:107], v[116:117], v[94:95]
	v_lshlrev_b32_e32 v106, 16, v20
	v_and_b32_e32 v107, 0xffff0000, v20
	v_and_b32_e32 v109, 0xffff0000, v96
	v_lshlrev_b32_e32 v114, 16, v56
	v_and_b32_e32 v115, 0xffff0000, v56
	v_pk_add_f32 v[108:109], v[108:109], v[106:107] neg_lo:[0,1] neg_hi:[0,1]
	v_lshlrev_b32_e32 v96, 16, v97
	v_pk_fma_f32 v[100:101], v[108:109], v[100:101], v[106:107]
	v_pk_add_f32 v[106:107], v[114:115], v[106:107] neg_lo:[0,1] neg_hi:[0,1]
	v_and_b32_e32 v97, 0xffff0000, v97
	v_pk_fma_f32 v[100:101], v[106:107], v[110:111], v[100:101]
	v_lshlrev_b32_e32 v106, 16, v21
	v_and_b32_e32 v107, 0xffff0000, v21
	v_lshlrev_b32_e32 v108, 16, v57
	v_and_b32_e32 v109, 0xffff0000, v57
	v_pk_add_f32 v[96:97], v[96:97], v[106:107] neg_lo:[0,1] neg_hi:[0,1]
	s_nop 0
	v_pk_fma_f32 v[96:97], v[96:97], v[102:103], v[106:107]
	v_pk_add_f32 v[102:103], v[108:109], v[106:107] neg_lo:[0,1] neg_hi:[0,1]
	s_nop 0
	v_pk_fma_f32 v[96:97], v[102:103], v[112:113], v[96:97]
	s_and_saveexec_b64 s[10:11], vcc
	s_xor_b64 s[10:11], exec, s[10:11]
	s_cbranch_execz .LBB0_681
	v_cmp_lt_u32_e32 vcc, s72, v130
	s_and_saveexec_b64 s[14:15], vcc
	s_xor_b64 s[14:15], exec, s[14:15]
	s_cbranch_execz .LBB0_678
	v_cmp_lt_u32_e32 vcc, s73, v130
	s_and_saveexec_b64 s[16:17], vcc
	s_xor_b64 s[16:17], exec, s[16:17]
	s_cbranch_execz .LBB0_675
	v_cmp_lt_u32_e32 vcc, s76, v130
	s_and_saveexec_b64 s[18:19], vcc
	s_xor_b64 s[18:19], exec, s[18:19]
	s_cbranch_execz .LBB0_640
	v_cmp_lt_u32_e32 vcc, s77, v130
	s_and_saveexec_b64 s[40:41], vcc
	s_cbranch_execz .LBB0_639
	v_mul_f32_e32 v102, 0xbfb8aa3b, v98
	v_exp_f32_e32 v98, v102
	s_nop 0
	v_mul_f32_e32 v102, 0xbfb8aa3b, v99
	v_exp_f32_e32 v99, v102
	s_nop 0
	v_pk_add_f32 v[98:99], v[98:99], 1.0 op_sel_hi:[1,0]
	v_mul_f32_e32 v102, 0xbfb8aa3b, v94
	v_exp_f32_e32 v94, v102
	s_nop 0
	v_mul_f32_e32 v102, 0xbfb8aa3b, v95
	v_exp_f32_e32 v95, v102
	s_nop 0
	v_pk_add_f32 v[94:95], v[94:95], 1.0 op_sel_hi:[1,0]
	v_mul_f32_e32 v102, 0xbfb8aa3b, v100
	v_exp_f32_e32 v100, v102
	s_nop 0
	v_mul_f32_e32 v102, 0xbfb8aa3b, v101
	v_exp_f32_e32 v101, v102
	s_nop 0
	v_pk_add_f32 v[100:101], v[100:101], 1.0 op_sel_hi:[1,0]
	v_mul_f32_e32 v102, 0xbfb8aa3b, v96
	v_exp_f32_e32 v96, v102
	s_nop 0
	v_mul_f32_e32 v102, 0xbfb8aa3b, v97
	v_exp_f32_e32 v97, v102
	s_nop 0
	v_div_scale_f32 v102, s[42:43], v98, v98, 1.0
	v_rcp_f32_e32 v103, v102
	v_pk_add_f32 v[96:97], v[96:97], 1.0 op_sel_hi:[1,0]
	v_fma_f32 v105, -v102, v103, 1.0
	v_fmac_f32_e32 v103, v105, v103
	v_div_scale_f32 v105, vcc, 1.0, v98, 1.0
	v_mul_f32_e32 v106, v105, v103
	v_fma_f32 v107, -v102, v106, v105
	v_fmac_f32_e32 v106, v107, v103
	v_fma_f32 v102, -v102, v106, v105
	v_div_fmas_f32 v102, v102, v103, v106
	v_div_fixup_f32 v98, v102, v98, 1.0
	v_rcp_f32_e32 v99, v99
	s_nop 3
	v_rcp_f32_e32 v94, v94
	s_nop 3
	v_rcp_f32_e32 v95, v95
	s_nop 3
	v_rcp_f32_e32 v100, v100
	s_nop 3
	v_rcp_f32_e32 v101, v101
	s_nop 3
	v_rcp_f32_e32 v96, v96
	s_nop 3
	v_div_scale_f32 v102, s[42:43], v97, v97, 1.0
	v_rcp_f32_e32 v103, v102
	s_nop 0
	v_fma_f32 v105, -v102, v103, 1.0
	v_fmac_f32_e32 v103, v105, v103
	v_div_scale_f32 v105, vcc, 1.0, v97, 1.0
	v_mul_f32_e32 v106, v105, v103
	v_fma_f32 v107, -v102, v106, v105
	v_fmac_f32_e32 v106, v107, v103
	v_fma_f32 v102, -v102, v106, v105
	v_div_fmas_f32 v102, v102, v103, v106
	v_div_fixup_f32 v97, v102, v97, 1.0

.LBB0_684:
	v_add_u32_e32 v130, v120, v150
	v_lshlrev_b64 v[94:95], 2, v[130:131]
	v_lshl_add_u64 v[102:103], s[22:23], 0, v[94:95]
	global_load_dwordx4 v[96:99], v[102:103], off offset:16
	s_nop 0
	global_load_dwordx4 v[102:105], v[102:103], off
	v_lshl_add_u64 v[94:95], s[28:29], 0, v[94:95]
	global_load_dwordx4 v[106:109], v[94:95], off offset:16
	global_load_dwordx4 v[110:113], v[94:95], off
	v_lshlrev_b32_e32 v94, 16, v22
	v_and_b32_e32 v95, 0xffff0000, v22
	v_lshlrev_b32_e32 v114, 16, v90
	v_and_b32_e32 v115, 0xffff0000, v90
	v_lshlrev_b32_e32 v116, 16, v62
	v_and_b32_e32 v117, 0xffff0000, v62
	v_pk_add_f32 v[114:115], v[114:115], v[94:95] neg_lo:[0,1] neg_hi:[0,1]
	v_lshlrev_b32_e32 v90, 16, v91
	v_and_b32_e32 v91, 0xffff0000, v91
	v_lshrrev_b32_e32 v100, 2, v151
	v_cmp_lt_u32_e32 vcc, s71, v130
	s_waitcnt vmcnt(2)
	v_pk_fma_f32 v[102:103], v[114:115], v[102:103], v[94:95]
	v_pk_add_f32 v[94:95], v[116:117], v[94:95] neg_lo:[0,1] neg_hi:[0,1]
	s_waitcnt vmcnt(0)
	v_pk_fma_f32 v[94:95], v[94:95], v[110:111], v[102:103]
	v_lshlrev_b32_e32 v102, 16, v23
	v_and_b32_e32 v103, 0xffff0000, v23
	v_lshlrev_b32_e32 v110, 16, v63
	v_and_b32_e32 v111, 0xffff0000, v63
	v_pk_add_f32 v[90:91], v[90:91], v[102:103] neg_lo:[0,1] neg_hi:[0,1]
	s_nop 0
	v_pk_fma_f32 v[90:91], v[90:91], v[104:105], v[102:103]
	v_pk_add_f32 v[102:103], v[110:111], v[102:103] neg_lo:[0,1] neg_hi:[0,1]
	v_lshlrev_b32_e32 v104, 16, v92
	v_pk_fma_f32 v[90:91], v[102:103], v[112:113], v[90:91]
	v_lshlrev_b32_e32 v102, 16, v24
	v_and_b32_e32 v103, 0xffff0000, v24
	v_and_b32_e32 v105, 0xffff0000, v92
	v_lshlrev_b32_e32 v110, 16, v64
	v_and_b32_e32 v111, 0xffff0000, v64
	v_pk_add_f32 v[104:105], v[104:105], v[102:103] neg_lo:[0,1] neg_hi:[0,1]
	v_lshlrev_b32_e32 v92, 16, v93
	v_pk_fma_f32 v[96:97], v[104:105], v[96:97], v[102:103]
	v_pk_add_f32 v[102:103], v[110:111], v[102:103] neg_lo:[0,1] neg_hi:[0,1]
	v_and_b32_e32 v93, 0xffff0000, v93
	v_pk_fma_f32 v[96:97], v[102:103], v[106:107], v[96:97]
	v_lshlrev_b32_e32 v102, 16, v25
	v_and_b32_e32 v103, 0xffff0000, v25
	v_lshlrev_b32_e32 v104, 16, v65
	v_and_b32_e32 v105, 0xffff0000, v65
	v_pk_add_f32 v[92:93], v[92:93], v[102:103] neg_lo:[0,1] neg_hi:[0,1]
	s_nop 0
	v_pk_fma_f32 v[92:93], v[92:93], v[98:99], v[102:103]
	v_pk_add_f32 v[98:99], v[104:105], v[102:103] neg_lo:[0,1] neg_hi:[0,1]
	s_nop 0
	v_pk_fma_f32 v[92:93], v[98:99], v[108:109], v[92:93]
	s_and_saveexec_b64 s[8:9], vcc
	s_xor_b64 s[8:9], exec, s[8:9]
	s_cbranch_execz .LBB0_732
	v_cmp_lt_u32_e32 vcc, s72, v130
	s_and_saveexec_b64 s[12:13], vcc
	s_xor_b64 s[12:13], exec, s[12:13]
	s_cbranch_execz .LBB0_729
	v_cmp_lt_u32_e32 vcc, s73, v130
	s_and_saveexec_b64 s[14:15], vcc
	s_xor_b64 s[14:15], exec, s[14:15]
	s_cbranch_execz .LBB0_726
	v_cmp_lt_u32_e32 vcc, s76, v130
	s_and_saveexec_b64 s[16:17], vcc
	s_xor_b64 s[16:17], exec, s[16:17]
	s_cbranch_execz .LBB0_691
	v_cmp_lt_u32_e32 vcc, s77, v130
	s_and_saveexec_b64 s[18:19], vcc
	s_cbranch_execz .LBB0_690
	v_mul_f32_e32 v98, 0xbfb8aa3b, v94
	v_exp_f32_e32 v94, v98
	s_nop 0
	v_mul_f32_e32 v98, 0xbfb8aa3b, v95
	v_exp_f32_e32 v95, v98
	s_nop 0
	v_pk_add_f32 v[94:95], v[94:95], 1.0 op_sel_hi:[1,0]
	v_mul_f32_e32 v98, 0xbfb8aa3b, v90
	v_exp_f32_e32 v90, v98
	s_nop 0
	v_mul_f32_e32 v98, 0xbfb8aa3b, v91
	v_exp_f32_e32 v91, v98
	s_nop 0
	v_pk_add_f32 v[90:91], v[90:91], 1.0 op_sel_hi:[1,0]
	v_mul_f32_e32 v98, 0xbfb8aa3b, v96
	v_exp_f32_e32 v96, v98
	s_nop 0
	v_mul_f32_e32 v98, 0xbfb8aa3b, v97
	v_exp_f32_e32 v97, v98
	s_nop 0
	v_pk_add_f32 v[96:97], v[96:97], 1.0 op_sel_hi:[1,0]
	v_mul_f32_e32 v98, 0xbfb8aa3b, v92
	v_exp_f32_e32 v92, v98
	s_nop 0
	v_mul_f32_e32 v98, 0xbfb8aa3b, v93
	v_exp_f32_e32 v93, v98
	s_nop 0
	v_div_scale_f32 v98, s[40:41], v94, v94, 1.0
	v_rcp_f32_e32 v99, v98
	v_pk_add_f32 v[92:93], v[92:93], 1.0 op_sel_hi:[1,0]
	v_fma_f32 v101, -v98, v99, 1.0
	v_fmac_f32_e32 v99, v101, v99
	v_div_scale_f32 v101, vcc, 1.0, v94, 1.0
	v_mul_f32_e32 v102, v101, v99
	v_fma_f32 v103, -v98, v102, v101
	v_fmac_f32_e32 v102, v103, v99
	v_fma_f32 v98, -v98, v102, v101
	v_div_fmas_f32 v98, v98, v99, v102
	v_div_fixup_f32 v94, v98, v94, 1.0
	v_rcp_f32_e32 v95, v95
	s_nop 3
	v_rcp_f32_e32 v90, v90
	s_nop 3
	v_rcp_f32_e32 v91, v91
	s_nop 3
	v_rcp_f32_e32 v96, v96
	s_nop 3
	v_rcp_f32_e32 v97, v97
	s_nop 3
	v_rcp_f32_e32 v92, v92
	s_nop 3
	v_div_scale_f32 v98, s[40:41], v93, v93, 1.0
	v_rcp_f32_e32 v99, v98
	s_nop 0
	v_fma_f32 v101, -v98, v99, 1.0
	v_fmac_f32_e32 v99, v101, v99
	v_div_scale_f32 v101, vcc, 1.0, v93, 1.0
	v_mul_f32_e32 v102, v101, v99
	v_fma_f32 v103, -v98, v102, v101
	v_fmac_f32_e32 v102, v103, v99
	v_fma_f32 v98, -v98, v102, v101
	v_div_fmas_f32 v98, v98, v99, v102
	v_div_fixup_f32 v93, v98, v93, 1.0

.LBB0_735:
	v_add_u32_e32 v130, v120, v147
	v_lshlrev_b64 v[90:91], 2, v[130:131]
	v_lshl_add_u64 v[98:99], s[22:23], 0, v[90:91]
	global_load_dwordx4 v[92:95], v[98:99], off offset:16
	s_nop 0
	global_load_dwordx4 v[98:101], v[98:99], off
	v_lshl_add_u64 v[90:91], s[28:29], 0, v[90:91]
	global_load_dwordx4 v[102:105], v[90:91], off offset:16
	global_load_dwordx4 v[106:109], v[90:91], off
	v_lshlrev_b32_e32 v90, 16, v26
	v_and_b32_e32 v91, 0xffff0000, v26
	v_lshlrev_b32_e32 v110, 16, v86
	v_and_b32_e32 v111, 0xffff0000, v86
	v_lshlrev_b32_e32 v112, 16, v70
	v_and_b32_e32 v113, 0xffff0000, v70
	v_pk_add_f32 v[110:111], v[110:111], v[90:91] neg_lo:[0,1] neg_hi:[0,1]
	v_lshlrev_b32_e32 v86, 16, v87
	v_and_b32_e32 v87, 0xffff0000, v87
	v_lshrrev_b32_e32 v96, 2, v148
	v_cmp_lt_u32_e32 vcc, s71, v130
	s_waitcnt vmcnt(2)
	v_pk_fma_f32 v[98:99], v[110:111], v[98:99], v[90:91]
	v_pk_add_f32 v[90:91], v[112:113], v[90:91] neg_lo:[0,1] neg_hi:[0,1]
	s_waitcnt vmcnt(0)
	v_pk_fma_f32 v[90:91], v[90:91], v[106:107], v[98:99]
	v_lshlrev_b32_e32 v98, 16, v27
	v_and_b32_e32 v99, 0xffff0000, v27
	v_lshlrev_b32_e32 v106, 16, v71
	v_and_b32_e32 v107, 0xffff0000, v71
	v_pk_add_f32 v[86:87], v[86:87], v[98:99] neg_lo:[0,1] neg_hi:[0,1]
	s_nop 0
	v_pk_fma_f32 v[86:87], v[86:87], v[100:101], v[98:99]
	v_pk_add_f32 v[98:99], v[106:107], v[98:99] neg_lo:[0,1] neg_hi:[0,1]
	v_lshlrev_b32_e32 v100, 16, v88
	v_pk_fma_f32 v[86:87], v[98:99], v[108:109], v[86:87]
	v_lshlrev_b32_e32 v98, 16, v28
	v_and_b32_e32 v99, 0xffff0000, v28
	v_and_b32_e32 v101, 0xffff0000, v88
	v_lshlrev_b32_e32 v106, 16, v72
	v_and_b32_e32 v107, 0xffff0000, v72
	v_pk_add_f32 v[100:101], v[100:101], v[98:99] neg_lo:[0,1] neg_hi:[0,1]
	v_lshlrev_b32_e32 v88, 16, v89
	v_pk_fma_f32 v[92:93], v[100:101], v[92:93], v[98:99]
	v_pk_add_f32 v[98:99], v[106:107], v[98:99] neg_lo:[0,1] neg_hi:[0,1]
	v_and_b32_e32 v89, 0xffff0000, v89
	v_pk_fma_f32 v[92:93], v[98:99], v[102:103], v[92:93]
	v_lshlrev_b32_e32 v98, 16, v29
	v_and_b32_e32 v99, 0xffff0000, v29
	v_lshlrev_b32_e32 v100, 16, v73
	v_and_b32_e32 v101, 0xffff0000, v73
	v_pk_add_f32 v[88:89], v[88:89], v[98:99] neg_lo:[0,1] neg_hi:[0,1]
	s_nop 0
	v_pk_fma_f32 v[88:89], v[88:89], v[94:95], v[98:99]
	v_pk_add_f32 v[94:95], v[100:101], v[98:99] neg_lo:[0,1] neg_hi:[0,1]
	s_nop 0
	v_pk_fma_f32 v[88:89], v[94:95], v[104:105], v[88:89]
	s_and_saveexec_b64 s[4:5], vcc
	s_xor_b64 s[4:5], exec, s[4:5]
	s_cbranch_execz .LBB0_783
	v_cmp_lt_u32_e32 vcc, s72, v130
	s_and_saveexec_b64 s[10:11], vcc
	s_xor_b64 s[10:11], exec, s[10:11]
	s_cbranch_execz .LBB0_780
	v_cmp_lt_u32_e32 vcc, s73, v130
	s_and_saveexec_b64 s[12:13], vcc
	s_xor_b64 s[12:13], exec, s[12:13]
	s_cbranch_execz .LBB0_777
	v_cmp_lt_u32_e32 vcc, s76, v130
	s_and_saveexec_b64 s[14:15], vcc
	s_xor_b64 s[14:15], exec, s[14:15]
	s_cbranch_execz .LBB0_742
	v_cmp_lt_u32_e32 vcc, s77, v130
	s_and_saveexec_b64 s[16:17], vcc
	s_cbranch_execz .LBB0_741
	v_mul_f32_e32 v94, 0xbfb8aa3b, v90
	v_exp_f32_e32 v90, v94
	s_nop 0
	v_mul_f32_e32 v94, 0xbfb8aa3b, v91
	v_exp_f32_e32 v91, v94
	s_nop 0
	v_pk_add_f32 v[90:91], v[90:91], 1.0 op_sel_hi:[1,0]
	v_mul_f32_e32 v94, 0xbfb8aa3b, v86
	v_exp_f32_e32 v86, v94
	s_nop 0
	v_mul_f32_e32 v94, 0xbfb8aa3b, v87
	v_exp_f32_e32 v87, v94
	s_nop 0
	v_pk_add_f32 v[86:87], v[86:87], 1.0 op_sel_hi:[1,0]
	v_mul_f32_e32 v94, 0xbfb8aa3b, v92
	v_exp_f32_e32 v92, v94
	s_nop 0
	v_mul_f32_e32 v94, 0xbfb8aa3b, v93
	v_exp_f32_e32 v93, v94
	s_nop 0
	v_pk_add_f32 v[92:93], v[92:93], 1.0 op_sel_hi:[1,0]
	v_mul_f32_e32 v94, 0xbfb8aa3b, v88
	v_exp_f32_e32 v88, v94
	s_nop 0
	v_mul_f32_e32 v94, 0xbfb8aa3b, v89
	v_exp_f32_e32 v89, v94
	s_nop 0
	v_div_scale_f32 v94, s[18:19], v90, v90, 1.0
	v_rcp_f32_e32 v95, v94
	v_pk_add_f32 v[88:89], v[88:89], 1.0 op_sel_hi:[1,0]
	v_fma_f32 v97, -v94, v95, 1.0
	v_fmac_f32_e32 v95, v97, v95
	v_div_scale_f32 v97, vcc, 1.0, v90, 1.0
	v_mul_f32_e32 v98, v97, v95
	v_fma_f32 v99, -v94, v98, v97
	v_fmac_f32_e32 v98, v99, v95
	v_fma_f32 v94, -v94, v98, v97
	v_div_fmas_f32 v94, v94, v95, v98
	v_div_fixup_f32 v90, v94, v90, 1.0
	v_rcp_f32_e32 v91, v91
	s_nop 3
	v_rcp_f32_e32 v86, v86
	s_nop 3
	v_rcp_f32_e32 v87, v87
	s_nop 3
	v_rcp_f32_e32 v92, v92
	s_nop 3
	v_rcp_f32_e32 v93, v93
	s_nop 3
	v_rcp_f32_e32 v88, v88
	s_nop 3
	v_div_scale_f32 v94, s[18:19], v89, v89, 1.0
	v_rcp_f32_e32 v95, v94
	s_nop 0
	v_fma_f32 v97, -v94, v95, 1.0
	v_fmac_f32_e32 v95, v97, v95
	v_div_scale_f32 v97, vcc, 1.0, v89, 1.0
	v_mul_f32_e32 v98, v97, v95
	v_fma_f32 v99, -v94, v98, v97
	v_fmac_f32_e32 v98, v99, v95
	v_fma_f32 v94, -v94, v98, v97
	v_div_fmas_f32 v94, v94, v95, v98
	v_div_fixup_f32 v89, v94, v89, 1.0

.LBB0_2690:
	s_or_b64 exec, exec, s[4:5]
	v_lshlrev_b64 v[132:133], 2, v[130:131]
	v_lshl_add_u64 v[126:127], s[28:29], 0, v[132:133]
	global_load_dwordx4 v[168:171], v[126:127], off offset:16
	s_nop 0
	global_load_dwordx4 v[126:129], v[126:127], off
	v_lshl_add_u64 v[132:133], s[36:37], 0, v[132:133]
	global_load_dwordx4 v[172:175], v[132:133], off offset:16
	global_load_dwordx4 v[176:179], v[132:133], off
	s_waitcnt vmcnt(4)
	v_lshlrev_b32_e32 v132, 16, v114
	v_and_b32_e32 v133, 0xffff0000, v114
	v_lshlrev_b32_e32 v180, 16, v118
	v_and_b32_e32 v181, 0xffff0000, v118
	v_lshlrev_b32_e32 v114, 16, v115
	v_and_b32_e32 v115, 0xffff0000, v115
	v_lshlrev_b32_e32 v118, 16, v119
	v_and_b32_e32 v119, 0xffff0000, v119
	v_lshlrev_b32_e32 v182, 16, v122
	v_and_b32_e32 v183, 0xffff0000, v122
	v_lshlrev_b32_e32 v122, 16, v123
	v_and_b32_e32 v123, 0xffff0000, v123
	v_pk_add_f32 v[118:119], v[118:119], v[114:115] neg_lo:[0,1] neg_hi:[0,1]
	v_pk_add_f32 v[180:181], v[180:181], v[132:133] neg_lo:[0,1] neg_hi:[0,1]
	v_cmp_lt_u32_e32 vcc, s76, v130
	s_waitcnt vmcnt(2)
	v_pk_fma_f32 v[118:119], v[118:119], v[128:129], v[114:115]
	v_pk_add_f32 v[114:115], v[122:123], v[114:115] neg_lo:[0,1] neg_hi:[0,1]
	v_lshlrev_b32_e32 v122, 16, v120
	s_waitcnt vmcnt(0)
	v_pk_fma_f32 v[114:115], v[114:115], v[178:179], v[118:119]
	v_lshlrev_b32_e32 v118, 16, v116
	v_and_b32_e32 v119, 0xffff0000, v116
	v_and_b32_e32 v123, 0xffff0000, v120
	v_lshlrev_b32_e32 v128, 16, v124
	v_and_b32_e32 v129, 0xffff0000, v124
	v_pk_add_f32 v[122:123], v[122:123], v[118:119] neg_lo:[0,1] neg_hi:[0,1]
	v_lshlrev_b32_e32 v116, 16, v117
	v_pk_fma_f32 v[122:123], v[122:123], v[168:169], v[118:119]
	v_pk_add_f32 v[118:119], v[128:129], v[118:119] neg_lo:[0,1] neg_hi:[0,1]
	v_and_b32_e32 v117, 0xffff0000, v117
	v_lshlrev_b32_e32 v120, 16, v121
	v_and_b32_e32 v121, 0xffff0000, v121
	v_pk_fma_f32 v[118:119], v[118:119], v[172:173], v[122:123]
	v_lshlrev_b32_e32 v122, 16, v125
	v_and_b32_e32 v123, 0xffff0000, v125
	v_pk_add_f32 v[120:121], v[120:121], v[116:117] neg_lo:[0,1] neg_hi:[0,1]
	v_pk_fma_f32 v[126:127], v[180:181], v[126:127], v[132:133]
	v_pk_add_f32 v[132:133], v[182:183], v[132:133] neg_lo:[0,1] neg_hi:[0,1]
	v_pk_fma_f32 v[120:121], v[120:121], v[170:171], v[116:117]
	v_pk_add_f32 v[116:117], v[122:123], v[116:117] neg_lo:[0,1] neg_hi:[0,1]
	v_pk_fma_f32 v[126:127], v[132:133], v[176:177], v[126:127]
	v_pk_fma_f32 v[116:117], v[116:117], v[174:175], v[120:121]
	s_and_saveexec_b64 s[2:3], vcc
	s_xor_b64 s[4:5], exec, s[2:3]
	s_cbranch_execz .LBB0_2738
	v_cmp_lt_u32_e32 vcc, s77, v130
	s_and_saveexec_b64 s[2:3], vcc
	s_xor_b64 s[46:47], exec, s[2:3]
	s_cbranch_execz .LBB0_2735
	v_cmp_lt_u32_e32 vcc, s78, v130
	s_and_saveexec_b64 s[2:3], vcc
	s_xor_b64 s[48:49], exec, s[2:3]
	s_cbranch_execz .LBB0_2732
	v_cmp_lt_u32_e32 vcc, s79, v130
	s_and_saveexec_b64 s[2:3], vcc
	s_xor_b64 s[50:51], exec, s[2:3]
	s_cbranch_execz .LBB0_2697
	v_cmp_lt_u32_e32 vcc, s80, v130
	s_and_saveexec_b64 s[52:53], vcc
	s_cbranch_execz .LBB0_2696
	v_mul_f32_e32 v120, 0xbfb8aa3b, v126
	v_rndne_f32_e32 v121, v120
	v_sub_f32_e32 v122, v120, v121
	v_fma_f32 v120, v126, s81, -v120
	v_fmac_f32_e32 v120, 0xb2a5705f, v126
	v_add_f32_e32 v120, v122, v120
	v_exp_f32_e32 v120, v120
	v_cvt_i32_f32_e32 v121, v121
	v_cmp_nlt_f32_e32 vcc, s82, v126
	v_ldexp_f32 v120, v120, v121
	v_mul_f32_e32 v121, 0xbfb8aa3b, v127
	v_rndne_f32_e32 v122, v121
	v_sub_f32_e32 v123, v121, v122
	v_fma_f32 v121, v127, s81, -v121
	v_fmac_f32_e32 v121, 0xb2a5705f, v127
	v_add_f32_e32 v121, v123, v121
	v_exp_f32_e32 v121, v121
	v_cvt_i32_f32_e32 v122, v122
	v_cndmask_b32_e32 v120, 0, v120, vcc
	v_cmp_ngt_f32_e32 vcc, s83, v126
	v_ldexp_f32 v121, v121, v122
	v_mul_f32_e32 v122, 0xbfb8aa3b, v114
	v_rndne_f32_e32 v123, v122
	v_sub_f32_e32 v124, v122, v123
	v_fma_f32 v122, v114, s81, -v122
	v_fmac_f32_e32 v122, 0xb2a5705f, v114
	v_add_f32_e32 v122, v124, v122
	v_exp_f32_e32 v122, v122
	v_cvt_i32_f32_e32 v123, v123
	v_cndmask_b32_e32 v120, v143, v120, vcc
	v_cmp_nlt_f32_e32 vcc, s82, v127
	v_ldexp_f32 v122, v122, v123
	s_nop 0
	v_cndmask_b32_e32 v121, 0, v121, vcc
	v_cmp_ngt_f32_e32 vcc, s83, v127
	s_nop 1
	v_cndmask_b32_e32 v121, v143, v121, vcc
	v_cmp_nlt_f32_e32 vcc, s82, v114
	v_pk_add_f32 v[120:121], v[120:121], 1.0 op_sel_hi:[1,0]
	s_nop 0
	v_cndmask_b32_e32 v122, 0, v122, vcc
	v_cmp_ngt_f32_e32 vcc, s83, v114
	s_nop 1
	v_cndmask_b32_e32 v114, v143, v122, vcc
	v_mul_f32_e32 v122, 0xbfb8aa3b, v115
	v_exp_f32_e32 v115, v122
	s_nop 0
	v_pk_add_f32 v[114:115], v[114:115], 1.0 op_sel_hi:[1,0]
	v_mul_f32_e32 v122, 0xbfb8aa3b, v118
	v_exp_f32_e32 v118, v122
	s_nop 0
	v_mul_f32_e32 v122, 0xbfb8aa3b, v119
	v_exp_f32_e32 v119, v122
	s_nop 0
	v_pk_add_f32 v[118:119], v[118:119], 1.0 op_sel_hi:[1,0]
	v_mul_f32_e32 v122, 0xbfb8aa3b, v116
	v_exp_f32_e32 v116, v122
	s_nop 0
	v_mul_f32_e32 v122, 0xbfb8aa3b, v117
	v_exp_f32_e32 v117, v122
	s_nop 0
	v_div_scale_f32 v122, s[2:3], v120, v120, 1.0
	v_rcp_f32_e32 v123, v122
	v_pk_add_f32 v[116:117], v[116:117], 1.0 op_sel_hi:[1,0]
	v_fma_f32 v124, -v122, v123, 1.0
	v_fmac_f32_e32 v123, v124, v123
	v_div_scale_f32 v124, vcc, 1.0, v120, 1.0
	v_mul_f32_e32 v125, v124, v123
	v_fma_f32 v126, -v122, v125, v124
	v_fmac_f32_e32 v125, v126, v123
	v_fma_f32 v122, -v122, v125, v124
	v_div_fmas_f32 v122, v122, v123, v125
	v_div_fixup_f32 v126, v122, v120, 1.0
	v_rcp_f32_e32 v127, v121
	s_nop 3
	v_rcp_f32_e32 v114, v114
	s_nop 3
	v_rcp_f32_e32 v115, v115
	s_nop 3
	v_rcp_f32_e32 v118, v118
	s_nop 3
	v_rcp_f32_e32 v119, v119
	s_nop 3
	v_rcp_f32_e32 v116, v116
	s_nop 3
	v_div_scale_f32 v120, s[2:3], v117, v117, 1.0
	v_rcp_f32_e32 v121, v120
	s_nop 0
	v_fma_f32 v122, -v120, v121, 1.0
	v_fmac_f32_e32 v121, v122, v121
	v_div_scale_f32 v122, vcc, 1.0, v117, 1.0
	v_mul_f32_e32 v123, v122, v121
	v_fma_f32 v124, -v120, v123, v122
	v_fmac_f32_e32 v123, v124, v121
	v_fma_f32 v120, -v120, v123, v122
	v_div_fmas_f32 v120, v120, v121, v123
	v_div_fixup_f32 v117, v120, v117, 1.0

.LBB0_2747:
	v_add_u32_e32 v130, v120, v165
	v_lshlrev_b64 v[114:115], 2, v[130:131]
	v_lshl_add_u64 v[122:123], s[28:29], 0, v[114:115]
	global_load_dwordx4 v[116:119], v[122:123], off offset:16
	s_nop 0
	global_load_dwordx4 v[122:125], v[122:123], off
	v_lshl_add_u64 v[114:115], s[36:37], 0, v[114:115]
	v_lshrrev_b32_e32 v121, 2, v166
	global_load_dwordx4 v[126:129], v[114:115], off offset:16
	global_load_dwordx4 v[164:167], v[114:115], off
	v_lshlrev_b32_e32 v114, 16, v10
	v_and_b32_e32 v115, 0xffff0000, v10
	v_lshlrev_b32_e32 v132, 16, v110
	v_and_b32_e32 v133, 0xffff0000, v110
	v_lshlrev_b32_e32 v168, 16, v38
	v_and_b32_e32 v169, 0xffff0000, v38
	v_pk_add_f32 v[132:133], v[132:133], v[114:115] neg_lo:[0,1] neg_hi:[0,1]
	v_lshlrev_b32_e32 v110, 16, v111
	v_and_b32_e32 v111, 0xffff0000, v111
	v_cmp_lt_u32_e32 vcc, s76, v130
	s_waitcnt vmcnt(2)
	v_pk_fma_f32 v[122:123], v[132:133], v[122:123], v[114:115]
	v_pk_add_f32 v[114:115], v[168:169], v[114:115] neg_lo:[0,1] neg_hi:[0,1]
	v_lshlrev_b32_e32 v132, 16, v39
	s_waitcnt vmcnt(0)
	v_pk_fma_f32 v[114:115], v[114:115], v[164:165], v[122:123]
	v_lshlrev_b32_e32 v122, 16, v11
	v_and_b32_e32 v123, 0xffff0000, v11
	v_and_b32_e32 v133, 0xffff0000, v39
	v_pk_add_f32 v[110:111], v[110:111], v[122:123] neg_lo:[0,1] neg_hi:[0,1]
	s_nop 0
	v_pk_fma_f32 v[110:111], v[110:111], v[124:125], v[122:123]
	v_pk_add_f32 v[122:123], v[132:133], v[122:123] neg_lo:[0,1] neg_hi:[0,1]
	v_lshlrev_b32_e32 v124, 16, v112
	v_pk_fma_f32 v[110:111], v[122:123], v[166:167], v[110:111]
	v_lshlrev_b32_e32 v122, 16, v12
	v_and_b32_e32 v123, 0xffff0000, v12
	v_and_b32_e32 v125, 0xffff0000, v112
	v_lshlrev_b32_e32 v132, 16, v40
	v_and_b32_e32 v133, 0xffff0000, v40
	v_pk_add_f32 v[124:125], v[124:125], v[122:123] neg_lo:[0,1] neg_hi:[0,1]
	v_lshlrev_b32_e32 v112, 16, v113
	v_pk_fma_f32 v[116:117], v[124:125], v[116:117], v[122:123]
	v_pk_add_f32 v[122:123], v[132:133], v[122:123] neg_lo:[0,1] neg_hi:[0,1]
	v_and_b32_e32 v113, 0xffff0000, v113
	v_pk_fma_f32 v[116:117], v[122:123], v[126:127], v[116:117]
	v_lshlrev_b32_e32 v122, 16, v13
	v_and_b32_e32 v123, 0xffff0000, v13
	v_lshlrev_b32_e32 v124, 16, v41
	v_and_b32_e32 v125, 0xffff0000, v41
	v_pk_add_f32 v[112:113], v[112:113], v[122:123] neg_lo:[0,1] neg_hi:[0,1]
	s_nop 0
	v_pk_fma_f32 v[112:113], v[112:113], v[118:119], v[122:123]
	v_pk_add_f32 v[118:119], v[124:125], v[122:123] neg_lo:[0,1] neg_hi:[0,1]
	s_nop 0
	v_pk_fma_f32 v[112:113], v[118:119], v[128:129], v[112:113]
	s_and_saveexec_b64 s[2:3], vcc
	s_xor_b64 s[22:23], exec, s[2:3]
	s_cbranch_execz .LBB0_2795
	v_cmp_lt_u32_e32 vcc, s77, v130
	s_and_saveexec_b64 s[2:3], vcc
	s_xor_b64 s[46:47], exec, s[2:3]
	s_cbranch_execz .LBB0_2792
	v_cmp_lt_u32_e32 vcc, s78, v130
	s_and_saveexec_b64 s[2:3], vcc
	s_xor_b64 s[48:49], exec, s[2:3]
	s_cbranch_execz .LBB0_2789
	v_cmp_lt_u32_e32 vcc, s79, v130
	s_and_saveexec_b64 s[2:3], vcc
	s_xor_b64 s[50:51], exec, s[2:3]
	s_cbranch_execz .LBB0_2754
	v_cmp_lt_u32_e32 vcc, s80, v130
	s_and_saveexec_b64 s[52:53], vcc
	s_cbranch_execz .LBB0_2753
	v_mul_f32_e32 v118, 0xbfb8aa3b, v114
	v_exp_f32_e32 v114, v118
	s_nop 0
	v_mul_f32_e32 v118, 0xbfb8aa3b, v115
	v_exp_f32_e32 v115, v118
	s_nop 0
	v_pk_add_f32 v[114:115], v[114:115], 1.0 op_sel_hi:[1,0]
	v_mul_f32_e32 v118, 0xbfb8aa3b, v110
	v_exp_f32_e32 v110, v118
	s_nop 0
	v_mul_f32_e32 v118, 0xbfb8aa3b, v111
	v_exp_f32_e32 v111, v118
	s_nop 0
	v_pk_add_f32 v[110:111], v[110:111], 1.0 op_sel_hi:[1,0]
	v_mul_f32_e32 v118, 0xbfb8aa3b, v116
	v_exp_f32_e32 v116, v118
	s_nop 0
	v_mul_f32_e32 v118, 0xbfb8aa3b, v117
	v_exp_f32_e32 v117, v118
	s_nop 0
	v_pk_add_f32 v[116:117], v[116:117], 1.0 op_sel_hi:[1,0]
	v_mul_f32_e32 v118, 0xbfb8aa3b, v112
	v_exp_f32_e32 v112, v118
	s_nop 0
	v_mul_f32_e32 v118, 0xbfb8aa3b, v113
	v_exp_f32_e32 v113, v118
	s_nop 0
	v_div_scale_f32 v118, s[2:3], v114, v114, 1.0
	v_rcp_f32_e32 v119, v118
	v_pk_add_f32 v[112:113], v[112:113], 1.0 op_sel_hi:[1,0]
	v_fma_f32 v122, -v118, v119, 1.0
	v_fmac_f32_e32 v119, v122, v119
	v_div_scale_f32 v122, vcc, 1.0, v114, 1.0
	v_mul_f32_e32 v123, v122, v119
	v_fma_f32 v124, -v118, v123, v122
	v_fmac_f32_e32 v123, v124, v119
	v_fma_f32 v118, -v118, v123, v122
	v_div_fmas_f32 v118, v118, v119, v123
	v_div_fixup_f32 v114, v118, v114, 1.0
	v_rcp_f32_e32 v115, v115
	s_nop 3
	v_rcp_f32_e32 v110, v110
	s_nop 3
	v_rcp_f32_e32 v111, v111
	s_nop 3
	v_rcp_f32_e32 v116, v116
	s_nop 3
	v_rcp_f32_e32 v117, v117
	s_nop 3
	v_rcp_f32_e32 v112, v112
	s_nop 3
	v_div_scale_f32 v118, s[2:3], v113, v113, 1.0
	v_rcp_f32_e32 v119, v118
	s_nop 0
	v_fma_f32 v122, -v118, v119, 1.0
	v_fmac_f32_e32 v119, v122, v119
	v_div_scale_f32 v122, vcc, 1.0, v113, 1.0
	v_mul_f32_e32 v123, v122, v119
	v_fma_f32 v124, -v118, v123, v122
	v_fmac_f32_e32 v123, v124, v119
	v_fma_f32 v118, -v118, v123, v122
	v_div_fmas_f32 v118, v118, v119, v123
	v_div_fixup_f32 v113, v118, v113, 1.0

.LBB0_2798:
	v_add_u32_e32 v130, v120, v162
	v_lshlrev_b64 v[110:111], 2, v[130:131]
	v_lshl_add_u64 v[118:119], s[28:29], 0, v[110:111]
	global_load_dwordx4 v[112:115], v[118:119], off offset:16
	global_load_dwordx4 v[122:125], v[118:119], off
	v_lshl_add_u64 v[110:111], s[36:37], 0, v[110:111]
	v_lshrrev_b32_e32 v116, 2, v163
	global_load_dwordx4 v[126:129], v[110:111], off offset:16
	global_load_dwordx4 v[162:165], v[110:111], off
	v_lshlrev_b32_e32 v110, 16, v6
	v_and_b32_e32 v111, 0xffff0000, v6
	v_lshlrev_b32_e32 v118, 16, v106
	v_and_b32_e32 v119, 0xffff0000, v106
	v_lshlrev_b32_e32 v132, 16, v34
	v_and_b32_e32 v133, 0xffff0000, v34
	v_pk_add_f32 v[118:119], v[118:119], v[110:111] neg_lo:[0,1] neg_hi:[0,1]
	v_lshlrev_b32_e32 v106, 16, v107
	v_and_b32_e32 v107, 0xffff0000, v107
	v_cmp_lt_u32_e32 vcc, s76, v130
	s_waitcnt vmcnt(2)
	v_pk_fma_f32 v[118:119], v[118:119], v[122:123], v[110:111]
	v_pk_add_f32 v[110:111], v[132:133], v[110:111] neg_lo:[0,1] neg_hi:[0,1]
	v_lshlrev_b32_e32 v122, 16, v35
	s_waitcnt vmcnt(0)
	v_pk_fma_f32 v[110:111], v[110:111], v[162:163], v[118:119]
	v_lshlrev_b32_e32 v118, 16, v7
	v_and_b32_e32 v119, 0xffff0000, v7
	v_and_b32_e32 v123, 0xffff0000, v35
	v_pk_add_f32 v[106:107], v[106:107], v[118:119] neg_lo:[0,1] neg_hi:[0,1]
	s_nop 0
	v_pk_fma_f32 v[106:107], v[106:107], v[124:125], v[118:119]
	v_pk_add_f32 v[118:119], v[122:123], v[118:119] neg_lo:[0,1] neg_hi:[0,1]
	v_lshlrev_b32_e32 v122, 16, v108
	v_pk_fma_f32 v[106:107], v[118:119], v[164:165], v[106:107]
	v_lshlrev_b32_e32 v118, 16, v8
	v_and_b32_e32 v119, 0xffff0000, v8
	v_and_b32_e32 v123, 0xffff0000, v108
	v_lshlrev_b32_e32 v124, 16, v36
	v_and_b32_e32 v125, 0xffff0000, v36
	v_pk_add_f32 v[122:123], v[122:123], v[118:119] neg_lo:[0,1] neg_hi:[0,1]
	v_lshlrev_b32_e32 v108, 16, v109
	v_pk_fma_f32 v[112:113], v[122:123], v[112:113], v[118:119]
	v_pk_add_f32 v[118:119], v[124:125], v[118:119] neg_lo:[0,1] neg_hi:[0,1]
	v_and_b32_e32 v109, 0xffff0000, v109
	v_pk_fma_f32 v[112:113], v[118:119], v[126:127], v[112:113]
	v_lshlrev_b32_e32 v118, 16, v9
	v_and_b32_e32 v119, 0xffff0000, v9
	v_lshlrev_b32_e32 v122, 16, v37
	v_and_b32_e32 v123, 0xffff0000, v37
	v_pk_add_f32 v[108:109], v[108:109], v[118:119] neg_lo:[0,1] neg_hi:[0,1]
	s_nop 0
	v_pk_fma_f32 v[108:109], v[108:109], v[114:115], v[118:119]
	v_pk_add_f32 v[114:115], v[122:123], v[118:119] neg_lo:[0,1] neg_hi:[0,1]
	s_nop 0
	v_pk_fma_f32 v[108:109], v[114:115], v[128:129], v[108:109]
	s_and_saveexec_b64 s[2:3], vcc
	s_xor_b64 s[20:21], exec, s[2:3]
	s_cbranch_execz .LBB0_2846
	v_cmp_lt_u32_e32 vcc, s77, v130
	s_and_saveexec_b64 s[2:3], vcc
	s_xor_b64 s[22:23], exec, s[2:3]
	s_cbranch_execz .LBB0_2843
	v_cmp_lt_u32_e32 vcc, s78, v130
	s_and_saveexec_b64 s[2:3], vcc
	s_xor_b64 s[46:47], exec, s[2:3]
	s_cbranch_execz .LBB0_2840
	v_cmp_lt_u32_e32 vcc, s79, v130
	s_and_saveexec_b64 s[2:3], vcc
	s_xor_b64 s[48:49], exec, s[2:3]
	s_cbranch_execz .LBB0_2805
	v_cmp_lt_u32_e32 vcc, s80, v130
	s_and_saveexec_b64 s[50:51], vcc
	s_cbranch_execz .LBB0_2804
	v_mul_f32_e32 v114, 0xbfb8aa3b, v110
	v_exp_f32_e32 v110, v114
	s_nop 0
	v_mul_f32_e32 v114, 0xbfb8aa3b, v111
	v_exp_f32_e32 v111, v114
	s_nop 0
	v_pk_add_f32 v[110:111], v[110:111], 1.0 op_sel_hi:[1,0]
	v_mul_f32_e32 v114, 0xbfb8aa3b, v106
	v_exp_f32_e32 v106, v114
	s_nop 0
	v_mul_f32_e32 v114, 0xbfb8aa3b, v107
	v_exp_f32_e32 v107, v114
	s_nop 0
	v_pk_add_f32 v[106:107], v[106:107], 1.0 op_sel_hi:[1,0]
	v_mul_f32_e32 v114, 0xbfb8aa3b, v112
	v_exp_f32_e32 v112, v114
	s_nop 0
	v_mul_f32_e32 v114, 0xbfb8aa3b, v113
	v_exp_f32_e32 v113, v114
	s_nop 0
	v_pk_add_f32 v[112:113], v[112:113], 1.0 op_sel_hi:[1,0]
	v_mul_f32_e32 v114, 0xbfb8aa3b, v108
	v_exp_f32_e32 v108, v114
	s_nop 0
	v_mul_f32_e32 v114, 0xbfb8aa3b, v109
	v_exp_f32_e32 v109, v114
	s_nop 0
	v_div_scale_f32 v114, s[2:3], v110, v110, 1.0
	v_rcp_f32_e32 v115, v114
	v_pk_add_f32 v[108:109], v[108:109], 1.0 op_sel_hi:[1,0]
	v_fma_f32 v117, -v114, v115, 1.0
	v_fmac_f32_e32 v115, v117, v115
	v_div_scale_f32 v117, vcc, 1.0, v110, 1.0
	v_mul_f32_e32 v118, v117, v115
	v_fma_f32 v119, -v114, v118, v117
	v_fmac_f32_e32 v118, v119, v115
	v_fma_f32 v114, -v114, v118, v117
	v_div_fmas_f32 v114, v114, v115, v118
	v_div_fixup_f32 v110, v114, v110, 1.0
	v_rcp_f32_e32 v111, v111
	s_nop 3
	v_rcp_f32_e32 v106, v106
	s_nop 3
	v_rcp_f32_e32 v107, v107
	s_nop 3
	v_rcp_f32_e32 v112, v112
	s_nop 3
	v_rcp_f32_e32 v113, v113
	s_nop 3
	v_rcp_f32_e32 v108, v108
	s_nop 3
	v_div_scale_f32 v114, s[2:3], v109, v109, 1.0
	v_rcp_f32_e32 v115, v114
	s_nop 0
	v_fma_f32 v117, -v114, v115, 1.0
	v_fmac_f32_e32 v115, v117, v115
	v_div_scale_f32 v117, vcc, 1.0, v109, 1.0
	v_mul_f32_e32 v118, v117, v115
	v_fma_f32 v119, -v114, v118, v117
	v_fmac_f32_e32 v118, v119, v115
	v_fma_f32 v114, -v114, v118, v117
	v_div_fmas_f32 v114, v114, v115, v118
	v_div_fixup_f32 v109, v114, v109, 1.0

.LBB0_2849:
	v_add_u32_e32 v130, v120, v159
	v_lshlrev_b64 v[106:107], 2, v[130:131]
	v_lshl_add_u64 v[114:115], s[28:29], 0, v[106:107]
	global_load_dwordx4 v[108:111], v[114:115], off offset:16
	s_nop 0
	global_load_dwordx4 v[114:117], v[114:115], off
	v_lshl_add_u64 v[106:107], s[36:37], 0, v[106:107]
	global_load_dwordx4 v[122:125], v[106:107], off offset:16
	global_load_dwordx4 v[126:129], v[106:107], off
	v_lshlrev_b32_e32 v106, 16, v2
	v_and_b32_e32 v107, 0xffff0000, v2
	v_lshlrev_b32_e32 v118, 16, v102
	v_and_b32_e32 v119, 0xffff0000, v102
	v_lshlrev_b32_e32 v132, 16, v30
	v_and_b32_e32 v133, 0xffff0000, v30
	v_pk_add_f32 v[118:119], v[118:119], v[106:107] neg_lo:[0,1] neg_hi:[0,1]
	v_lshlrev_b32_e32 v102, 16, v103
	v_and_b32_e32 v103, 0xffff0000, v103
	v_lshrrev_b32_e32 v112, 2, v160
	v_cmp_lt_u32_e32 vcc, s76, v130
	s_waitcnt vmcnt(2)
	v_pk_fma_f32 v[114:115], v[118:119], v[114:115], v[106:107]
	v_pk_add_f32 v[106:107], v[132:133], v[106:107] neg_lo:[0,1] neg_hi:[0,1]
	v_lshlrev_b32_e32 v118, 16, v31
	s_waitcnt vmcnt(0)
	v_pk_fma_f32 v[106:107], v[106:107], v[126:127], v[114:115]
	v_lshlrev_b32_e32 v114, 16, v3
	v_and_b32_e32 v115, 0xffff0000, v3
	v_and_b32_e32 v119, 0xffff0000, v31
	v_pk_add_f32 v[102:103], v[102:103], v[114:115] neg_lo:[0,1] neg_hi:[0,1]
	s_nop 0
	v_pk_fma_f32 v[102:103], v[102:103], v[116:117], v[114:115]
	v_pk_add_f32 v[114:115], v[118:119], v[114:115] neg_lo:[0,1] neg_hi:[0,1]
	v_lshlrev_b32_e32 v116, 16, v104
	v_pk_fma_f32 v[102:103], v[114:115], v[128:129], v[102:103]
	v_lshlrev_b32_e32 v114, 16, v4
	v_and_b32_e32 v115, 0xffff0000, v4
	v_and_b32_e32 v117, 0xffff0000, v104
	v_lshlrev_b32_e32 v118, 16, v32
	v_and_b32_e32 v119, 0xffff0000, v32
	v_pk_add_f32 v[116:117], v[116:117], v[114:115] neg_lo:[0,1] neg_hi:[0,1]
	v_lshlrev_b32_e32 v104, 16, v105
	v_pk_fma_f32 v[108:109], v[116:117], v[108:109], v[114:115]
	v_pk_add_f32 v[114:115], v[118:119], v[114:115] neg_lo:[0,1] neg_hi:[0,1]
	v_and_b32_e32 v105, 0xffff0000, v105
	v_pk_fma_f32 v[108:109], v[114:115], v[122:123], v[108:109]
	v_lshlrev_b32_e32 v114, 16, v5
	v_and_b32_e32 v115, 0xffff0000, v5
	v_lshlrev_b32_e32 v116, 16, v33
	v_and_b32_e32 v117, 0xffff0000, v33
	v_pk_add_f32 v[104:105], v[104:105], v[114:115] neg_lo:[0,1] neg_hi:[0,1]
	s_nop 0
	v_pk_fma_f32 v[104:105], v[104:105], v[110:111], v[114:115]
	v_pk_add_f32 v[110:111], v[116:117], v[114:115] neg_lo:[0,1] neg_hi:[0,1]
	s_nop 0
	v_pk_fma_f32 v[104:105], v[110:111], v[124:125], v[104:105]
	s_and_saveexec_b64 s[2:3], vcc
	s_xor_b64 s[18:19], exec, s[2:3]
	s_cbranch_execz .LBB0_2897
	v_cmp_lt_u32_e32 vcc, s77, v130
	s_and_saveexec_b64 s[2:3], vcc
	s_xor_b64 s[20:21], exec, s[2:3]
	s_cbranch_execz .LBB0_2894
	v_cmp_lt_u32_e32 vcc, s78, v130
	s_and_saveexec_b64 s[2:3], vcc
	s_xor_b64 s[22:23], exec, s[2:3]
	s_cbranch_execz .LBB0_2891
	v_cmp_lt_u32_e32 vcc, s79, v130
	s_and_saveexec_b64 s[2:3], vcc
	s_xor_b64 s[46:47], exec, s[2:3]
	s_cbranch_execz .LBB0_2856
	v_cmp_lt_u32_e32 vcc, s80, v130
	s_and_saveexec_b64 s[48:49], vcc
	s_cbranch_execz .LBB0_2855
	v_mul_f32_e32 v110, 0xbfb8aa3b, v106
	v_exp_f32_e32 v106, v110
	s_nop 0
	v_mul_f32_e32 v110, 0xbfb8aa3b, v107
	v_exp_f32_e32 v107, v110
	s_nop 0
	v_pk_add_f32 v[106:107], v[106:107], 1.0 op_sel_hi:[1,0]
	v_mul_f32_e32 v110, 0xbfb8aa3b, v102
	v_exp_f32_e32 v102, v110
	s_nop 0
	v_mul_f32_e32 v110, 0xbfb8aa3b, v103
	v_exp_f32_e32 v103, v110
	s_nop 0
	v_pk_add_f32 v[102:103], v[102:103], 1.0 op_sel_hi:[1,0]
	v_mul_f32_e32 v110, 0xbfb8aa3b, v108
	v_exp_f32_e32 v108, v110
	s_nop 0
	v_mul_f32_e32 v110, 0xbfb8aa3b, v109
	v_exp_f32_e32 v109, v110
	s_nop 0
	v_pk_add_f32 v[108:109], v[108:109], 1.0 op_sel_hi:[1,0]
	v_mul_f32_e32 v110, 0xbfb8aa3b, v104
	v_exp_f32_e32 v104, v110
	s_nop 0
	v_mul_f32_e32 v110, 0xbfb8aa3b, v105
	v_exp_f32_e32 v105, v110
	s_nop 0
	v_div_scale_f32 v110, s[2:3], v106, v106, 1.0
	v_rcp_f32_e32 v111, v110
	v_pk_add_f32 v[104:105], v[104:105], 1.0 op_sel_hi:[1,0]
	v_fma_f32 v113, -v110, v111, 1.0
	v_fmac_f32_e32 v111, v113, v111
	v_div_scale_f32 v113, vcc, 1.0, v106, 1.0
	v_mul_f32_e32 v114, v113, v111
	v_fma_f32 v115, -v110, v114, v113
	v_fmac_f32_e32 v114, v115, v111
	v_fma_f32 v110, -v110, v114, v113
	v_div_fmas_f32 v110, v110, v111, v114
	v_div_fixup_f32 v106, v110, v106, 1.0
	v_rcp_f32_e32 v107, v107
	s_nop 3
	v_rcp_f32_e32 v102, v102
	s_nop 3
	v_rcp_f32_e32 v103, v103
	s_nop 3
	v_rcp_f32_e32 v108, v108
	s_nop 3
	v_rcp_f32_e32 v109, v109
	s_nop 3
	v_rcp_f32_e32 v104, v104
	s_nop 3
	v_div_scale_f32 v110, s[2:3], v105, v105, 1.0
	v_rcp_f32_e32 v111, v110
	s_nop 0
	v_fma_f32 v113, -v110, v111, 1.0
	v_fmac_f32_e32 v111, v113, v111
	v_div_scale_f32 v113, vcc, 1.0, v105, 1.0
	v_mul_f32_e32 v114, v113, v111
	v_fma_f32 v115, -v110, v114, v113
	v_fmac_f32_e32 v114, v115, v111
	v_fma_f32 v110, -v110, v114, v113
	v_div_fmas_f32 v110, v110, v111, v114
	v_div_fixup_f32 v105, v110, v105, 1.0

.LBB0_2900:
	v_add_u32_e32 v130, v120, v156
	v_lshlrev_b64 v[102:103], 2, v[130:131]
	v_lshl_add_u64 v[110:111], s[28:29], 0, v[102:103]
	global_load_dwordx4 v[104:107], v[110:111], off offset:16
	s_nop 0
	global_load_dwordx4 v[110:113], v[110:111], off
	v_lshl_add_u64 v[102:103], s[36:37], 0, v[102:103]
	global_load_dwordx4 v[114:117], v[102:103], off offset:16
	global_load_dwordx4 v[122:125], v[102:103], off
	v_lshlrev_b32_e32 v102, 16, v14
	v_and_b32_e32 v103, 0xffff0000, v14
	v_lshlrev_b32_e32 v118, 16, v98
	v_and_b32_e32 v119, 0xffff0000, v98
	v_lshlrev_b32_e32 v126, 16, v46
	v_and_b32_e32 v127, 0xffff0000, v46
	v_pk_add_f32 v[118:119], v[118:119], v[102:103] neg_lo:[0,1] neg_hi:[0,1]
	v_lshlrev_b32_e32 v98, 16, v99
	v_and_b32_e32 v99, 0xffff0000, v99
	v_lshrrev_b32_e32 v108, 2, v157
	v_cmp_lt_u32_e32 vcc, s76, v130
	s_waitcnt vmcnt(2)
	v_pk_fma_f32 v[110:111], v[118:119], v[110:111], v[102:103]
	v_pk_add_f32 v[102:103], v[126:127], v[102:103] neg_lo:[0,1] neg_hi:[0,1]
	v_lshlrev_b32_e32 v118, 16, v47
	s_waitcnt vmcnt(0)
	v_pk_fma_f32 v[102:103], v[102:103], v[122:123], v[110:111]
	v_lshlrev_b32_e32 v110, 16, v15
	v_and_b32_e32 v111, 0xffff0000, v15
	v_and_b32_e32 v119, 0xffff0000, v47
	v_pk_add_f32 v[98:99], v[98:99], v[110:111] neg_lo:[0,1] neg_hi:[0,1]
	s_nop 0
	v_pk_fma_f32 v[98:99], v[98:99], v[112:113], v[110:111]
	v_pk_add_f32 v[110:111], v[118:119], v[110:111] neg_lo:[0,1] neg_hi:[0,1]
	v_lshlrev_b32_e32 v112, 16, v100
	v_pk_fma_f32 v[98:99], v[110:111], v[124:125], v[98:99]
	v_lshlrev_b32_e32 v110, 16, v16
	v_and_b32_e32 v111, 0xffff0000, v16
	v_and_b32_e32 v113, 0xffff0000, v100
	v_lshlrev_b32_e32 v118, 16, v48
	v_and_b32_e32 v119, 0xffff0000, v48
	v_pk_add_f32 v[112:113], v[112:113], v[110:111] neg_lo:[0,1] neg_hi:[0,1]
	v_lshlrev_b32_e32 v100, 16, v101
	v_pk_fma_f32 v[104:105], v[112:113], v[104:105], v[110:111]
	v_pk_add_f32 v[110:111], v[118:119], v[110:111] neg_lo:[0,1] neg_hi:[0,1]
	v_and_b32_e32 v101, 0xffff0000, v101
	v_pk_fma_f32 v[104:105], v[110:111], v[114:115], v[104:105]
	v_lshlrev_b32_e32 v110, 16, v17
	v_and_b32_e32 v111, 0xffff0000, v17
	v_lshlrev_b32_e32 v112, 16, v49
	v_and_b32_e32 v113, 0xffff0000, v49
	v_pk_add_f32 v[100:101], v[100:101], v[110:111] neg_lo:[0,1] neg_hi:[0,1]
	s_nop 0
	v_pk_fma_f32 v[100:101], v[100:101], v[106:107], v[110:111]
	v_pk_add_f32 v[106:107], v[112:113], v[110:111] neg_lo:[0,1] neg_hi:[0,1]
	s_nop 0
	v_pk_fma_f32 v[100:101], v[106:107], v[116:117], v[100:101]
	s_and_saveexec_b64 s[2:3], vcc
	s_xor_b64 s[16:17], exec, s[2:3]
	s_cbranch_execz .LBB0_2948
	v_cmp_lt_u32_e32 vcc, s77, v130
	s_and_saveexec_b64 s[2:3], vcc
	s_xor_b64 s[18:19], exec, s[2:3]
	s_cbranch_execz .LBB0_2945
	v_cmp_lt_u32_e32 vcc, s78, v130
	s_and_saveexec_b64 s[2:3], vcc
	s_xor_b64 s[20:21], exec, s[2:3]
	s_cbranch_execz .LBB0_2942
	v_cmp_lt_u32_e32 vcc, s79, v130
	s_and_saveexec_b64 s[2:3], vcc
	s_xor_b64 s[22:23], exec, s[2:3]
	s_cbranch_execz .LBB0_2907
	v_cmp_lt_u32_e32 vcc, s80, v130
	s_and_saveexec_b64 s[46:47], vcc
	s_cbranch_execz .LBB0_2906
	v_mul_f32_e32 v106, 0xbfb8aa3b, v102
	v_exp_f32_e32 v102, v106
	s_nop 0
	v_mul_f32_e32 v106, 0xbfb8aa3b, v103
	v_exp_f32_e32 v103, v106
	s_nop 0
	v_pk_add_f32 v[102:103], v[102:103], 1.0 op_sel_hi:[1,0]
	v_mul_f32_e32 v106, 0xbfb8aa3b, v98
	v_exp_f32_e32 v98, v106
	s_nop 0
	v_mul_f32_e32 v106, 0xbfb8aa3b, v99
	v_exp_f32_e32 v99, v106
	s_nop 0
	v_pk_add_f32 v[98:99], v[98:99], 1.0 op_sel_hi:[1,0]
	v_mul_f32_e32 v106, 0xbfb8aa3b, v104
	v_exp_f32_e32 v104, v106
	s_nop 0
	v_mul_f32_e32 v106, 0xbfb8aa3b, v105
	v_exp_f32_e32 v105, v106
	s_nop 0
	v_pk_add_f32 v[104:105], v[104:105], 1.0 op_sel_hi:[1,0]
	v_mul_f32_e32 v106, 0xbfb8aa3b, v100
	v_exp_f32_e32 v100, v106
	s_nop 0
	v_mul_f32_e32 v106, 0xbfb8aa3b, v101
	v_exp_f32_e32 v101, v106
	s_nop 0
	v_div_scale_f32 v106, s[2:3], v102, v102, 1.0
	v_rcp_f32_e32 v107, v106
	v_pk_add_f32 v[100:101], v[100:101], 1.0 op_sel_hi:[1,0]
	v_fma_f32 v109, -v106, v107, 1.0
	v_fmac_f32_e32 v107, v109, v107
	v_div_scale_f32 v109, vcc, 1.0, v102, 1.0
	v_mul_f32_e32 v110, v109, v107
	v_fma_f32 v111, -v106, v110, v109
	v_fmac_f32_e32 v110, v111, v107
	v_fma_f32 v106, -v106, v110, v109
	v_div_fmas_f32 v106, v106, v107, v110
	v_div_fixup_f32 v102, v106, v102, 1.0
	v_rcp_f32_e32 v103, v103
	s_nop 3
	v_rcp_f32_e32 v98, v98
	s_nop 3
	v_rcp_f32_e32 v99, v99
	s_nop 3
	v_rcp_f32_e32 v104, v104
	s_nop 3
	v_rcp_f32_e32 v105, v105
	s_nop 3
	v_rcp_f32_e32 v100, v100
	s_nop 3
	v_div_scale_f32 v106, s[2:3], v101, v101, 1.0
	v_rcp_f32_e32 v107, v106
	s_nop 0
	v_fma_f32 v109, -v106, v107, 1.0
	v_fmac_f32_e32 v107, v109, v107
	v_div_scale_f32 v109, vcc, 1.0, v101, 1.0
	v_mul_f32_e32 v110, v109, v107
	v_fma_f32 v111, -v106, v110, v109
	v_fmac_f32_e32 v110, v111, v107
	v_fma_f32 v106, -v106, v110, v109
	v_div_fmas_f32 v106, v106, v107, v110
	v_div_fixup_f32 v101, v106, v101, 1.0

.LBB0_2951:
	v_add_u32_e32 v130, v120, v153
	v_lshlrev_b64 v[98:99], 2, v[130:131]
	v_lshl_add_u64 v[106:107], s[28:29], 0, v[98:99]
	global_load_dwordx4 v[100:103], v[106:107], off offset:16
	s_nop 0
	global_load_dwordx4 v[106:109], v[106:107], off
	v_lshl_add_u64 v[98:99], s[36:37], 0, v[98:99]
	global_load_dwordx4 v[110:113], v[98:99], off offset:16
	global_load_dwordx4 v[114:117], v[98:99], off
	v_lshlrev_b32_e32 v98, 16, v18
	v_and_b32_e32 v99, 0xffff0000, v18
	v_lshlrev_b32_e32 v118, 16, v94
	v_and_b32_e32 v119, 0xffff0000, v94
	v_lshlrev_b32_e32 v122, 16, v54
	v_and_b32_e32 v123, 0xffff0000, v54
	v_pk_add_f32 v[118:119], v[118:119], v[98:99] neg_lo:[0,1] neg_hi:[0,1]
	v_lshlrev_b32_e32 v94, 16, v95
	v_and_b32_e32 v95, 0xffff0000, v95
	v_lshrrev_b32_e32 v104, 2, v154
	v_cmp_lt_u32_e32 vcc, s76, v130
	s_waitcnt vmcnt(2)
	v_pk_fma_f32 v[106:107], v[118:119], v[106:107], v[98:99]
	v_pk_add_f32 v[98:99], v[122:123], v[98:99] neg_lo:[0,1] neg_hi:[0,1]
	s_waitcnt vmcnt(0)
	v_pk_fma_f32 v[98:99], v[98:99], v[114:115], v[106:107]
	v_lshlrev_b32_e32 v106, 16, v19
	v_and_b32_e32 v107, 0xffff0000, v19
	v_lshlrev_b32_e32 v114, 16, v55
	v_and_b32_e32 v115, 0xffff0000, v55
	v_pk_add_f32 v[94:95], v[94:95], v[106:107] neg_lo:[0,1] neg_hi:[0,1]
	s_nop 0
	v_pk_fma_f32 v[94:95], v[94:95], v[108:109], v[106:107]
	v_pk_add_f32 v[106:107], v[114:115], v[106:107] neg_lo:[0,1] neg_hi:[0,1]
	v_lshlrev_b32_e32 v108, 16, v96
	v_pk_fma_f32 v[94:95], v[106:107], v[116:117], v[94:95]
	v_lshlrev_b32_e32 v106, 16, v20
	v_and_b32_e32 v107, 0xffff0000, v20
	v_and_b32_e32 v109, 0xffff0000, v96
	v_lshlrev_b32_e32 v114, 16, v56
	v_and_b32_e32 v115, 0xffff0000, v56
	v_pk_add_f32 v[108:109], v[108:109], v[106:107] neg_lo:[0,1] neg_hi:[0,1]
	v_lshlrev_b32_e32 v96, 16, v97
	v_pk_fma_f32 v[100:101], v[108:109], v[100:101], v[106:107]
	v_pk_add_f32 v[106:107], v[114:115], v[106:107] neg_lo:[0,1] neg_hi:[0,1]
	v_and_b32_e32 v97, 0xffff0000, v97
	v_pk_fma_f32 v[100:101], v[106:107], v[110:111], v[100:101]
	v_lshlrev_b32_e32 v106, 16, v21
	v_and_b32_e32 v107, 0xffff0000, v21
	v_lshlrev_b32_e32 v108, 16, v57
	v_and_b32_e32 v109, 0xffff0000, v57
	v_pk_add_f32 v[96:97], v[96:97], v[106:107] neg_lo:[0,1] neg_hi:[0,1]
	s_nop 0
	v_pk_fma_f32 v[96:97], v[96:97], v[102:103], v[106:107]
	v_pk_add_f32 v[102:103], v[108:109], v[106:107] neg_lo:[0,1] neg_hi:[0,1]
	s_nop 0
	v_pk_fma_f32 v[96:97], v[102:103], v[112:113], v[96:97]
	s_and_saveexec_b64 s[2:3], vcc
	s_xor_b64 s[14:15], exec, s[2:3]
	s_cbranch_execz .LBB0_2999
	v_cmp_lt_u32_e32 vcc, s77, v130
	s_and_saveexec_b64 s[2:3], vcc
	s_xor_b64 s[16:17], exec, s[2:3]
	s_cbranch_execz .LBB0_2996
	v_cmp_lt_u32_e32 vcc, s78, v130
	s_and_saveexec_b64 s[2:3], vcc
	s_xor_b64 s[18:19], exec, s[2:3]
	s_cbranch_execz .LBB0_2993
	v_cmp_lt_u32_e32 vcc, s79, v130
	s_and_saveexec_b64 s[2:3], vcc
	s_xor_b64 s[20:21], exec, s[2:3]
	s_cbranch_execz .LBB0_2958
	v_cmp_lt_u32_e32 vcc, s80, v130
	s_and_saveexec_b64 s[22:23], vcc
	s_cbranch_execz .LBB0_2957
	v_mul_f32_e32 v102, 0xbfb8aa3b, v98
	v_exp_f32_e32 v98, v102
	s_nop 0
	v_mul_f32_e32 v102, 0xbfb8aa3b, v99
	v_exp_f32_e32 v99, v102
	s_nop 0
	v_pk_add_f32 v[98:99], v[98:99], 1.0 op_sel_hi:[1,0]
	v_mul_f32_e32 v102, 0xbfb8aa3b, v94
	v_exp_f32_e32 v94, v102
	s_nop 0
	v_mul_f32_e32 v102, 0xbfb8aa3b, v95
	v_exp_f32_e32 v95, v102
	s_nop 0
	v_pk_add_f32 v[94:95], v[94:95], 1.0 op_sel_hi:[1,0]
	v_mul_f32_e32 v102, 0xbfb8aa3b, v100
	v_exp_f32_e32 v100, v102
	s_nop 0
	v_mul_f32_e32 v102, 0xbfb8aa3b, v101
	v_exp_f32_e32 v101, v102
	s_nop 0
	v_pk_add_f32 v[100:101], v[100:101], 1.0 op_sel_hi:[1,0]
	v_mul_f32_e32 v102, 0xbfb8aa3b, v96
	v_exp_f32_e32 v96, v102
	s_nop 0
	v_mul_f32_e32 v102, 0xbfb8aa3b, v97
	v_exp_f32_e32 v97, v102
	s_nop 0
	v_div_scale_f32 v102, s[2:3], v98, v98, 1.0
	v_rcp_f32_e32 v103, v102
	v_pk_add_f32 v[96:97], v[96:97], 1.0 op_sel_hi:[1,0]
	v_fma_f32 v105, -v102, v103, 1.0
	v_fmac_f32_e32 v103, v105, v103
	v_div_scale_f32 v105, vcc, 1.0, v98, 1.0
	v_mul_f32_e32 v106, v105, v103
	v_fma_f32 v107, -v102, v106, v105
	v_fmac_f32_e32 v106, v107, v103
	v_fma_f32 v102, -v102, v106, v105
	v_div_fmas_f32 v102, v102, v103, v106
	v_div_fixup_f32 v98, v102, v98, 1.0
	v_rcp_f32_e32 v99, v99
	s_nop 3
	v_rcp_f32_e32 v94, v94
	s_nop 3
	v_rcp_f32_e32 v95, v95
	s_nop 3
	v_rcp_f32_e32 v100, v100
	s_nop 3
	v_rcp_f32_e32 v101, v101
	s_nop 3
	v_rcp_f32_e32 v96, v96
	s_nop 3
	v_div_scale_f32 v102, s[2:3], v97, v97, 1.0
	v_rcp_f32_e32 v103, v102
	s_nop 0
	v_fma_f32 v105, -v102, v103, 1.0
	v_fmac_f32_e32 v103, v105, v103
	v_div_scale_f32 v105, vcc, 1.0, v97, 1.0
	v_mul_f32_e32 v106, v105, v103
	v_fma_f32 v107, -v102, v106, v105
	v_fmac_f32_e32 v106, v107, v103
	v_fma_f32 v102, -v102, v106, v105
	v_div_fmas_f32 v102, v102, v103, v106
	v_div_fixup_f32 v97, v102, v97, 1.0

.LBB0_3002:
	v_add_u32_e32 v130, v120, v150
	v_lshlrev_b64 v[94:95], 2, v[130:131]
	v_lshl_add_u64 v[102:103], s[28:29], 0, v[94:95]
	global_load_dwordx4 v[96:99], v[102:103], off offset:16
	s_nop 0
	global_load_dwordx4 v[102:105], v[102:103], off
	v_lshl_add_u64 v[94:95], s[36:37], 0, v[94:95]
	global_load_dwordx4 v[106:109], v[94:95], off offset:16
	global_load_dwordx4 v[110:113], v[94:95], off
	v_lshlrev_b32_e32 v94, 16, v22
	v_and_b32_e32 v95, 0xffff0000, v22
	v_lshlrev_b32_e32 v114, 16, v90
	v_and_b32_e32 v115, 0xffff0000, v90
	v_lshlrev_b32_e32 v116, 16, v62
	v_and_b32_e32 v117, 0xffff0000, v62
	v_pk_add_f32 v[114:115], v[114:115], v[94:95] neg_lo:[0,1] neg_hi:[0,1]
	v_lshlrev_b32_e32 v90, 16, v91
	v_and_b32_e32 v91, 0xffff0000, v91
	v_lshrrev_b32_e32 v100, 2, v151
	v_cmp_lt_u32_e32 vcc, s76, v130
	s_waitcnt vmcnt(2)
	v_pk_fma_f32 v[102:103], v[114:115], v[102:103], v[94:95]
	v_pk_add_f32 v[94:95], v[116:117], v[94:95] neg_lo:[0,1] neg_hi:[0,1]
	s_waitcnt vmcnt(0)
	v_pk_fma_f32 v[94:95], v[94:95], v[110:111], v[102:103]
	v_lshlrev_b32_e32 v102, 16, v23
	v_and_b32_e32 v103, 0xffff0000, v23
	v_lshlrev_b32_e32 v110, 16, v63
	v_and_b32_e32 v111, 0xffff0000, v63
	v_pk_add_f32 v[90:91], v[90:91], v[102:103] neg_lo:[0,1] neg_hi:[0,1]
	s_nop 0
	v_pk_fma_f32 v[90:91], v[90:91], v[104:105], v[102:103]
	v_pk_add_f32 v[102:103], v[110:111], v[102:103] neg_lo:[0,1] neg_hi:[0,1]
	v_lshlrev_b32_e32 v104, 16, v92
	v_pk_fma_f32 v[90:91], v[102:103], v[112:113], v[90:91]
	v_lshlrev_b32_e32 v102, 16, v24
	v_and_b32_e32 v103, 0xffff0000, v24
	v_and_b32_e32 v105, 0xffff0000, v92
	v_lshlrev_b32_e32 v110, 16, v64
	v_and_b32_e32 v111, 0xffff0000, v64
	v_pk_add_f32 v[104:105], v[104:105], v[102:103] neg_lo:[0,1] neg_hi:[0,1]
	v_lshlrev_b32_e32 v92, 16, v93
	v_pk_fma_f32 v[96:97], v[104:105], v[96:97], v[102:103]
	v_pk_add_f32 v[102:103], v[110:111], v[102:103] neg_lo:[0,1] neg_hi:[0,1]
	v_and_b32_e32 v93, 0xffff0000, v93
	v_pk_fma_f32 v[96:97], v[102:103], v[106:107], v[96:97]
	v_lshlrev_b32_e32 v102, 16, v25
	v_and_b32_e32 v103, 0xffff0000, v25
	v_lshlrev_b32_e32 v104, 16, v65
	v_and_b32_e32 v105, 0xffff0000, v65
	v_pk_add_f32 v[92:93], v[92:93], v[102:103] neg_lo:[0,1] neg_hi:[0,1]
	s_nop 0
	v_pk_fma_f32 v[92:93], v[92:93], v[98:99], v[102:103]
	v_pk_add_f32 v[98:99], v[104:105], v[102:103] neg_lo:[0,1] neg_hi:[0,1]
	s_nop 0
	v_pk_fma_f32 v[92:93], v[98:99], v[108:109], v[92:93]
	s_and_saveexec_b64 s[2:3], vcc
	s_xor_b64 s[12:13], exec, s[2:3]
	s_cbranch_execz .LBB0_3050
	v_cmp_lt_u32_e32 vcc, s77, v130
	s_and_saveexec_b64 s[2:3], vcc
	s_xor_b64 s[14:15], exec, s[2:3]
	s_cbranch_execz .LBB0_3047
	v_cmp_lt_u32_e32 vcc, s78, v130
	s_and_saveexec_b64 s[2:3], vcc
	s_xor_b64 s[16:17], exec, s[2:3]
	s_cbranch_execz .LBB0_3044
	v_cmp_lt_u32_e32 vcc, s79, v130
	s_and_saveexec_b64 s[2:3], vcc
	s_xor_b64 s[18:19], exec, s[2:3]
	s_cbranch_execz .LBB0_3009
	v_cmp_lt_u32_e32 vcc, s80, v130
	s_and_saveexec_b64 s[20:21], vcc
	s_cbranch_execz .LBB0_3008
	v_mul_f32_e32 v98, 0xbfb8aa3b, v94
	v_exp_f32_e32 v94, v98
	s_nop 0
	v_mul_f32_e32 v98, 0xbfb8aa3b, v95
	v_exp_f32_e32 v95, v98
	s_nop 0
	v_pk_add_f32 v[94:95], v[94:95], 1.0 op_sel_hi:[1,0]
	v_mul_f32_e32 v98, 0xbfb8aa3b, v90
	v_exp_f32_e32 v90, v98
	s_nop 0
	v_mul_f32_e32 v98, 0xbfb8aa3b, v91
	v_exp_f32_e32 v91, v98
	s_nop 0
	v_pk_add_f32 v[90:91], v[90:91], 1.0 op_sel_hi:[1,0]
	v_mul_f32_e32 v98, 0xbfb8aa3b, v96
	v_exp_f32_e32 v96, v98
	s_nop 0
	v_mul_f32_e32 v98, 0xbfb8aa3b, v97
	v_exp_f32_e32 v97, v98
	s_nop 0
	v_pk_add_f32 v[96:97], v[96:97], 1.0 op_sel_hi:[1,0]
	v_mul_f32_e32 v98, 0xbfb8aa3b, v92
	v_exp_f32_e32 v92, v98
	s_nop 0
	v_mul_f32_e32 v98, 0xbfb8aa3b, v93
	v_exp_f32_e32 v93, v98
	s_nop 0
	v_div_scale_f32 v98, s[2:3], v94, v94, 1.0
	v_rcp_f32_e32 v99, v98
	v_pk_add_f32 v[92:93], v[92:93], 1.0 op_sel_hi:[1,0]
	v_fma_f32 v101, -v98, v99, 1.0
	v_fmac_f32_e32 v99, v101, v99
	v_div_scale_f32 v101, vcc, 1.0, v94, 1.0
	v_mul_f32_e32 v102, v101, v99
	v_fma_f32 v103, -v98, v102, v101
	v_fmac_f32_e32 v102, v103, v99
	v_fma_f32 v98, -v98, v102, v101
	v_div_fmas_f32 v98, v98, v99, v102
	v_div_fixup_f32 v94, v98, v94, 1.0
	v_rcp_f32_e32 v95, v95
	s_nop 3
	v_rcp_f32_e32 v90, v90
	s_nop 3
	v_rcp_f32_e32 v91, v91
	s_nop 3
	v_rcp_f32_e32 v96, v96
	s_nop 3
	v_rcp_f32_e32 v97, v97
	s_nop 3
	v_rcp_f32_e32 v92, v92
	s_nop 3
	v_div_scale_f32 v98, s[2:3], v93, v93, 1.0
	v_rcp_f32_e32 v99, v98
	s_nop 0
	v_fma_f32 v101, -v98, v99, 1.0
	v_fmac_f32_e32 v99, v101, v99
	v_div_scale_f32 v101, vcc, 1.0, v93, 1.0
	v_mul_f32_e32 v102, v101, v99
	v_fma_f32 v103, -v98, v102, v101
	v_fmac_f32_e32 v102, v103, v99
	v_fma_f32 v98, -v98, v102, v101
	v_div_fmas_f32 v98, v98, v99, v102
	v_div_fixup_f32 v93, v98, v93, 1.0

.LBB0_3053:
	v_add_u32_e32 v130, v120, v147
	v_lshlrev_b64 v[90:91], 2, v[130:131]
	v_lshl_add_u64 v[98:99], s[28:29], 0, v[90:91]
	global_load_dwordx4 v[92:95], v[98:99], off offset:16
	s_nop 0
	global_load_dwordx4 v[98:101], v[98:99], off
	v_lshl_add_u64 v[90:91], s[36:37], 0, v[90:91]
	global_load_dwordx4 v[102:105], v[90:91], off offset:16
	global_load_dwordx4 v[106:109], v[90:91], off
	v_lshlrev_b32_e32 v90, 16, v26
	v_and_b32_e32 v91, 0xffff0000, v26
	v_lshlrev_b32_e32 v110, 16, v86
	v_and_b32_e32 v111, 0xffff0000, v86
	v_lshlrev_b32_e32 v112, 16, v70
	v_and_b32_e32 v113, 0xffff0000, v70
	v_pk_add_f32 v[110:111], v[110:111], v[90:91] neg_lo:[0,1] neg_hi:[0,1]
	v_lshlrev_b32_e32 v86, 16, v87
	v_and_b32_e32 v87, 0xffff0000, v87
	v_lshrrev_b32_e32 v96, 2, v148
	v_cmp_lt_u32_e32 vcc, s76, v130
	s_waitcnt vmcnt(2)
	v_pk_fma_f32 v[98:99], v[110:111], v[98:99], v[90:91]
	v_pk_add_f32 v[90:91], v[112:113], v[90:91] neg_lo:[0,1] neg_hi:[0,1]
	s_waitcnt vmcnt(0)
	v_pk_fma_f32 v[90:91], v[90:91], v[106:107], v[98:99]
	v_lshlrev_b32_e32 v98, 16, v27
	v_and_b32_e32 v99, 0xffff0000, v27
	v_lshlrev_b32_e32 v106, 16, v71
	v_and_b32_e32 v107, 0xffff0000, v71
	v_pk_add_f32 v[86:87], v[86:87], v[98:99] neg_lo:[0,1] neg_hi:[0,1]
	s_nop 0
	v_pk_fma_f32 v[86:87], v[86:87], v[100:101], v[98:99]
	v_pk_add_f32 v[98:99], v[106:107], v[98:99] neg_lo:[0,1] neg_hi:[0,1]
	v_lshlrev_b32_e32 v100, 16, v88
	v_pk_fma_f32 v[86:87], v[98:99], v[108:109], v[86:87]
	v_lshlrev_b32_e32 v98, 16, v28
	v_and_b32_e32 v99, 0xffff0000, v28
	v_and_b32_e32 v101, 0xffff0000, v88
	v_lshlrev_b32_e32 v106, 16, v72
	v_and_b32_e32 v107, 0xffff0000, v72
	v_pk_add_f32 v[100:101], v[100:101], v[98:99] neg_lo:[0,1] neg_hi:[0,1]
	v_lshlrev_b32_e32 v88, 16, v89
	v_pk_fma_f32 v[92:93], v[100:101], v[92:93], v[98:99]
	v_pk_add_f32 v[98:99], v[106:107], v[98:99] neg_lo:[0,1] neg_hi:[0,1]
	v_and_b32_e32 v89, 0xffff0000, v89
	v_pk_fma_f32 v[92:93], v[98:99], v[102:103], v[92:93]
	v_lshlrev_b32_e32 v98, 16, v29
	v_and_b32_e32 v99, 0xffff0000, v29
	v_lshlrev_b32_e32 v100, 16, v73
	v_and_b32_e32 v101, 0xffff0000, v73
	v_pk_add_f32 v[88:89], v[88:89], v[98:99] neg_lo:[0,1] neg_hi:[0,1]
	s_nop 0
	v_pk_fma_f32 v[88:89], v[88:89], v[94:95], v[98:99]
	v_pk_add_f32 v[94:95], v[100:101], v[98:99] neg_lo:[0,1] neg_hi:[0,1]
	s_nop 0
	v_pk_fma_f32 v[88:89], v[94:95], v[104:105], v[88:89]
	s_and_saveexec_b64 s[2:3], vcc
	s_xor_b64 s[6:7], exec, s[2:3]
	s_cbranch_execz .LBB0_3101
	v_cmp_lt_u32_e32 vcc, s77, v130
	s_and_saveexec_b64 s[2:3], vcc
	s_xor_b64 s[12:13], exec, s[2:3]
	s_cbranch_execz .LBB0_3098
	v_cmp_lt_u32_e32 vcc, s78, v130
	s_and_saveexec_b64 s[2:3], vcc
	s_xor_b64 s[14:15], exec, s[2:3]
	s_cbranch_execz .LBB0_3095
	v_cmp_lt_u32_e32 vcc, s79, v130
	s_and_saveexec_b64 s[2:3], vcc
	s_xor_b64 s[16:17], exec, s[2:3]
	s_cbranch_execz .LBB0_3060
	v_cmp_lt_u32_e32 vcc, s80, v130
	s_and_saveexec_b64 s[18:19], vcc
	s_cbranch_execz .LBB0_3059
	v_mul_f32_e32 v94, 0xbfb8aa3b, v90
	v_exp_f32_e32 v90, v94
	s_nop 0
	v_mul_f32_e32 v94, 0xbfb8aa3b, v91
	v_exp_f32_e32 v91, v94
	s_nop 0
	v_pk_add_f32 v[90:91], v[90:91], 1.0 op_sel_hi:[1,0]
	v_mul_f32_e32 v94, 0xbfb8aa3b, v86
	v_exp_f32_e32 v86, v94
	s_nop 0
	v_mul_f32_e32 v94, 0xbfb8aa3b, v87
	v_exp_f32_e32 v87, v94
	s_nop 0
	v_pk_add_f32 v[86:87], v[86:87], 1.0 op_sel_hi:[1,0]
	v_mul_f32_e32 v94, 0xbfb8aa3b, v92
	v_exp_f32_e32 v92, v94
	s_nop 0
	v_mul_f32_e32 v94, 0xbfb8aa3b, v93
	v_exp_f32_e32 v93, v94
	s_nop 0
	v_pk_add_f32 v[92:93], v[92:93], 1.0 op_sel_hi:[1,0]
	v_mul_f32_e32 v94, 0xbfb8aa3b, v88
	v_exp_f32_e32 v88, v94
	s_nop 0
	v_mul_f32_e32 v94, 0xbfb8aa3b, v89
	v_exp_f32_e32 v89, v94
	s_nop 0
	v_div_scale_f32 v94, s[2:3], v90, v90, 1.0
	v_rcp_f32_e32 v95, v94
	v_pk_add_f32 v[88:89], v[88:89], 1.0 op_sel_hi:[1,0]
	v_fma_f32 v97, -v94, v95, 1.0
	v_fmac_f32_e32 v95, v97, v95
	v_div_scale_f32 v97, vcc, 1.0, v90, 1.0
	v_mul_f32_e32 v98, v97, v95
	v_fma_f32 v99, -v94, v98, v97
	v_fmac_f32_e32 v98, v99, v95
	v_fma_f32 v94, -v94, v98, v97
	v_div_fmas_f32 v94, v94, v95, v98
	v_div_fixup_f32 v90, v94, v90, 1.0
	v_rcp_f32_e32 v91, v91
	s_nop 3
	v_rcp_f32_e32 v86, v86
	s_nop 3
	v_rcp_f32_e32 v87, v87
	s_nop 3
	v_rcp_f32_e32 v92, v92
	s_nop 3
	v_rcp_f32_e32 v93, v93
	s_nop 3
	v_rcp_f32_e32 v88, v88
	s_nop 3
	v_div_scale_f32 v94, s[2:3], v89, v89, 1.0
	v_rcp_f32_e32 v95, v94
	s_nop 0
	v_fma_f32 v97, -v94, v95, 1.0
	v_fmac_f32_e32 v95, v97, v95
	v_div_scale_f32 v97, vcc, 1.0, v89, 1.0
	v_mul_f32_e32 v98, v97, v95
	v_fma_f32 v99, -v94, v98, v97
	v_fmac_f32_e32 v98, v99, v95
	v_fma_f32 v94, -v94, v98, v97
	v_div_fmas_f32 v94, v94, v95, v98
	v_div_fixup_f32 v89, v94, v89, 1.0
